# added section barriers guarded by the original workgroup-uniform trip test (robust to non-divisible token counts)
# speedup vs baseline: 1.0607x; 1.0048x over previous
;     ...
;     for (int t = F.gw; t < T; t += F.ngw) {
;         int xh[4], xl[4]; float xdq, mean1, rstd1;
;         {
;             const v4u hq = *(const v4u*)(F.ws + WS_XQ + (size_t)t * 2048 + lane * 32), lq = *(const v4u*)(F.ws + WS_XQ + (size_t)t * 2048 + lane * 32 + 16);
;             const f32x4 r4 = *(const f32x4*)(F.ws + WS_R4 + (size_t)t * 16);
;             xh[0] = (int)hq.x; xh[1] = (int)hq.y; xh[2] = (int)hq.z; xh[3] = (int)hq.w; xl[0] = (int)lq.x; xl[1] = (int)lq.y; xl[2] = (int)lq.z; xl[3] = (int)lq.w;
;             xdq = r4[0]; mean1 = r4[1]; rstd1 = r4[2];
;         }
;         if (t - F.wave + (NWAVES - 1) < T) __syncthreads();
.LBB0_1416:
	v_readlane_b32 s62, v254, 58
	s_ashr_i32 s89, s62, 31
	s_mov_b32 s88, s62
	s_lshl_b64 s[86:87], s[88:89], 11
	s_lshl_b64 s[56:57], s[88:89], 4
	v_lshl_add_u64 v[66:67], v[132:133], 0, s[86:87]
	s_add_u32 s56, s30, s56
	global_load_dwordx4 v[70:73], v[66:67], off offset:16
	s_addc_u32 s57, s39, s57
	global_load_dwordx4 v[74:77], v[66:67], off
	s_nop 0
	global_load_dwordx3 v[66:68], v1, s[56:57]
	v_readlane_b32 s56, v254, 55
	s_sub_i32 s56, s62, s56
	s_cmpk_gt_i32 s56, 0x3ff8
	s_cselect_b32 s101, 0, 1
	v_readlane_b32 s63, v254, 59
	s_cbranch_scc1 .LBB0_1418
	s_waitcnt lgkmcnt(0)
	s_barrier

.LBB0_1419:
	v_mov_b32_e32 v69, v1
	v_mov_b32_e32 v83, v1
	s_waitcnt vmcnt(6)
	v_dot8c_i32_i4_e32 v69, v6, v74
	v_dot8c_i32_i4_e32 v83, v6, v70
	v_dot8c_i32_i4_e32 v69, v7, v75
	v_dot8c_i32_i4_e32 v83, v7, v71
	s_add_i32 s62, s57, -15
	v_dot8c_i32_i4_e32 v69, v8, v76
	v_dot8c_i32_i4_e32 v83, v8, v72
	s_cmp_lt_u32 s56, 3
	v_dot8c_i32_i4_e32 v69, v9, v77
	v_dot8c_i32_i4_e32 v83, v9, v73
	s_cselect_b64 vcc, -1, 0
	s_nop 1
	v_lshl_add_u32 v6, v69, 4, v83
	v_cndmask_b32_e32 v83, v79, v78, vcc
	v_cvt_f32_i32_e32 v69, v6
	v_readlane_b32 s62, v83, s62
	s_lshl_b32 s62, s62, 10
	s_nop 3
	buffer_load_dwordx4 v[6:9], v0, s[92:95], s62 offen
	v_mov_b32_e32 v84, v1
	v_mov_b32_e32 v85, v1
	s_waitcnt vmcnt(6)
	v_dot8c_i32_i4_e32 v84, v14, v74
	v_dot8c_i32_i4_e32 v85, v14, v70
	v_dot8c_i32_i4_e32 v84, v15, v75
	v_dot8c_i32_i4_e32 v85, v15, v71
	v_dot8c_i32_i4_e32 v84, v16, v76
	v_dot8c_i32_i4_e32 v85, v16, v72
	s_add_i32 s62, s57, -14
	v_dot8c_i32_i4_e32 v84, v17, v77
	v_dot8c_i32_i4_e32 v85, v17, v73
	v_readlane_b32 s62, v83, s62
	s_lshl_b32 s62, s62, 10
	s_nop 0
	v_lshl_add_u32 v14, v84, 4, v85
	v_cvt_f32_i32_e32 v84, v14
	s_nop 0
	buffer_load_dwordx4 v[14:17], v0, s[92:95], s62 offen
	v_mov_b32_e32 v85, v1
	v_mov_b32_e32 v86, v1
	s_waitcnt vmcnt(6)
	v_dot8c_i32_i4_e32 v85, v30, v74
	v_dot8c_i32_i4_e32 v86, v30, v70
	v_dot8c_i32_i4_e32 v85, v31, v75
	v_dot8c_i32_i4_e32 v86, v31, v71
	v_dot8c_i32_i4_e32 v85, v32, v76
	v_dot8c_i32_i4_e32 v86, v32, v72
	s_add_i32 s62, s57, -13
	v_dot8c_i32_i4_e32 v85, v33, v77
	v_dot8c_i32_i4_e32 v86, v33, v73
	v_readlane_b32 s62, v83, s62
	s_lshl_b32 s62, s62, 10
	s_nop 0
	v_lshl_add_u32 v30, v85, 4, v86
	v_cvt_f32_i32_e32 v85, v30
	s_nop 0
	buffer_load_dwordx4 v[30:33], v0, s[92:95], s62 offen
	v_mov_b32_e32 v86, v1
	v_mov_b32_e32 v87, v1
	s_waitcnt vmcnt(6)
	v_dot8c_i32_i4_e32 v86, v46, v74
	v_dot8c_i32_i4_e32 v87, v46, v70
	v_dot8c_i32_i4_e32 v86, v47, v75
	v_dot8c_i32_i4_e32 v87, v47, v71
	v_dot8c_i32_i4_e32 v86, v48, v76
	v_dot8c_i32_i4_e32 v87, v48, v72
	s_add_i32 s62, s57, -12
	v_dot8c_i32_i4_e32 v86, v49, v77
	v_dot8c_i32_i4_e32 v87, v49, v73
	v_readlane_b32 s62, v83, s62
	s_lshl_b32 s62, s62, 10
	s_nop 0
	v_lshl_add_u32 v46, v86, 4, v87
	v_cvt_f32_i32_e32 v86, v46
	s_nop 0
	buffer_load_dwordx4 v[46:49], v0, s[92:95], s62 offen
	v_mov_b32_e32 v87, v1
	v_mov_b32_e32 v88, v1
	s_waitcnt vmcnt(6)
	v_dot8c_i32_i4_e32 v87, v2, v74
	v_dot8c_i32_i4_e32 v88, v2, v70
	v_dot8c_i32_i4_e32 v87, v3, v75
	v_dot8c_i32_i4_e32 v88, v3, v71
	v_dot8c_i32_i4_e32 v87, v4, v76
	v_dot8c_i32_i4_e32 v88, v4, v72
	s_add_i32 s62, s57, -11
	v_dot8c_i32_i4_e32 v87, v5, v77
	v_dot8c_i32_i4_e32 v88, v5, v73
	v_readlane_b32 s62, v83, s62
	s_lshl_b32 s62, s62, 10
	s_nop 0
	v_lshl_add_u32 v2, v87, 4, v88
	v_cvt_f32_i32_e32 v87, v2
	s_nop 0
	buffer_load_dwordx4 v[2:5], v0, s[92:95], s62 offen
	v_mov_b32_e32 v88, v1
	v_mov_b32_e32 v89, v1
	s_waitcnt vmcnt(6)
	v_dot8c_i32_i4_e32 v88, v22, v74
	v_dot8c_i32_i4_e32 v89, v22, v70
	v_dot8c_i32_i4_e32 v88, v23, v75
	v_dot8c_i32_i4_e32 v89, v23, v71
	v_dot8c_i32_i4_e32 v88, v24, v76
	v_dot8c_i32_i4_e32 v89, v24, v72
	s_add_i32 s62, s57, -10
	v_dot8c_i32_i4_e32 v88, v25, v77
	v_dot8c_i32_i4_e32 v89, v25, v73
	v_readlane_b32 s62, v83, s62
	s_lshl_b32 s62, s62, 10
	s_nop 0
	v_lshl_add_u32 v22, v88, 4, v89
	v_cvt_f32_i32_e32 v88, v22
	s_nop 0
	buffer_load_dwordx4 v[22:25], v0, s[92:95], s62 offen
	v_mov_b32_e32 v89, v1
	v_mov_b32_e32 v90, v1
	s_waitcnt vmcnt(6)
	v_dot8c_i32_i4_e32 v89, v38, v74
	v_dot8c_i32_i4_e32 v90, v38, v70
	v_dot8c_i32_i4_e32 v89, v39, v75
	v_dot8c_i32_i4_e32 v90, v39, v71
	v_dot8c_i32_i4_e32 v89, v40, v76
	v_dot8c_i32_i4_e32 v90, v40, v72
	s_add_i32 s62, s57, -9
	v_dot8c_i32_i4_e32 v89, v41, v77
	v_dot8c_i32_i4_e32 v90, v41, v73
	v_readlane_b32 s62, v83, s62
	s_lshl_b32 s62, s62, 10
	s_nop 0
	v_lshl_add_u32 v38, v89, 4, v90
	v_cvt_f32_i32_e32 v89, v38
	s_nop 0
	buffer_load_dwordx4 v[38:41], v0, s[92:95], s62 offen
	v_mov_b32_e32 v90, v1
	v_mov_b32_e32 v91, v1
	s_waitcnt vmcnt(6)
	v_dot8c_i32_i4_e32 v90, v54, v74
	v_dot8c_i32_i4_e32 v91, v54, v70
	v_dot8c_i32_i4_e32 v90, v55, v75
	v_dot8c_i32_i4_e32 v91, v55, v71
	v_dot8c_i32_i4_e32 v90, v56, v76
	v_dot8c_i32_i4_e32 v91, v56, v72
	s_add_i32 s62, s57, -8
	v_dot8c_i32_i4_e32 v90, v57, v77
	v_dot8c_i32_i4_e32 v91, v57, v73
	v_readlane_b32 s62, v83, s62
	s_lshl_b32 s62, s62, 10
	s_nop 0
	v_lshl_add_u32 v54, v90, 4, v91
	v_cvt_f32_i32_e32 v90, v54
	s_nop 0
	buffer_load_dwordx4 v[54:57], v0, s[92:95], s62 offen
	v_mov_b32_e32 v91, v1
	v_mov_b32_e32 v92, v1
	s_waitcnt vmcnt(6)
	v_dot8c_i32_i4_e32 v91, v10, v74
	v_dot8c_i32_i4_e32 v92, v10, v70
	v_dot8c_i32_i4_e32 v91, v11, v75
	v_dot8c_i32_i4_e32 v92, v11, v71
	v_dot8c_i32_i4_e32 v91, v12, v76
	v_dot8c_i32_i4_e32 v92, v12, v72
	s_add_i32 s62, s57, -7
	v_dot8c_i32_i4_e32 v91, v13, v77
	v_dot8c_i32_i4_e32 v92, v13, v73
	v_readlane_b32 s62, v83, s62
	s_lshl_b32 s62, s62, 10
	s_nop 0
	v_lshl_add_u32 v10, v91, 4, v92
	v_cvt_f32_i32_e32 v91, v10
	s_nop 0
	buffer_load_dwordx4 v[10:13], v0, s[92:95], s62 offen
	v_mov_b32_e32 v92, v1
	v_mov_b32_e32 v93, v1
	s_waitcnt vmcnt(6)
	v_dot8c_i32_i4_e32 v92, v26, v74
	v_dot8c_i32_i4_e32 v93, v26, v70
	v_dot8c_i32_i4_e32 v92, v27, v75
	v_dot8c_i32_i4_e32 v93, v27, v71
	v_dot8c_i32_i4_e32 v92, v28, v76
	v_dot8c_i32_i4_e32 v93, v28, v72
	s_add_i32 s62, s57, -6
	v_dot8c_i32_i4_e32 v92, v29, v77
	v_dot8c_i32_i4_e32 v93, v29, v73
	v_readlane_b32 s62, v83, s62
	s_lshl_b32 s62, s62, 10
	s_nop 0
	v_lshl_add_u32 v26, v92, 4, v93
	v_cvt_f32_i32_e32 v92, v26
	s_nop 0
	buffer_load_dwordx4 v[26:29], v0, s[92:95], s62 offen
	v_mov_b32_e32 v93, v1
	v_mov_b32_e32 v94, v1
	s_waitcnt vmcnt(6)
; __device__ __forceinline__ float gelu_as(float v) {
;     const float av = fabsf(v), t = __builtin_amdgcn_rcpf(av * 0.2316418882f + 1.0f);
;     float q = t * 0.5307027145f + (-0.7265760135f); q = q * t + 0.7107068705f; q = q * t + (-0.142248368f); q = q * t + 0.127414796f; q = q * t;
;     const float m = v * (q * __builtin_amdgcn_exp2f((v * v) * (-0.72134752044f)));
;     return v < 0.f ? m : v - m;
; }
	v_dot8c_i32_i4_e32 v93, v42, v74
	v_dot8c_i32_i4_e32 v94, v42, v70
	v_dot8c_i32_i4_e32 v93, v43, v75
	v_dot8c_i32_i4_e32 v94, v43, v71
	v_dot8c_i32_i4_e32 v93, v44, v76
	v_dot8c_i32_i4_e32 v94, v44, v72
	s_add_i32 s62, s57, -5
	v_dot8c_i32_i4_e32 v93, v45, v77
	v_dot8c_i32_i4_e32 v94, v45, v73
	v_readlane_b32 s62, v83, s62
	s_lshl_b32 s62, s62, 10
	s_nop 0
	v_lshl_add_u32 v42, v93, 4, v94
	v_cvt_f32_i32_e32 v93, v42
	s_nop 0
	buffer_load_dwordx4 v[42:45], v0, s[92:95], s62 offen
	v_mov_b32_e32 v94, v1
	v_mov_b32_e32 v95, v1
	s_waitcnt vmcnt(6)
	v_dot8c_i32_i4_e32 v94, v58, v74
	v_dot8c_i32_i4_e32 v95, v58, v70
	v_dot8c_i32_i4_e32 v94, v59, v75
	v_dot8c_i32_i4_e32 v95, v59, v71
	v_dot8c_i32_i4_e32 v94, v60, v76
	v_dot8c_i32_i4_e32 v95, v60, v72
	s_add_i32 s62, s57, -4
	v_dot8c_i32_i4_e32 v94, v61, v77
	v_dot8c_i32_i4_e32 v95, v61, v73
	v_readlane_b32 s62, v83, s62
	s_lshl_b32 s62, s62, 10
	s_nop 0
	v_lshl_add_u32 v58, v94, 4, v95
	v_cvt_f32_i32_e32 v94, v58
	s_nop 0
	buffer_load_dwordx4 v[58:61], v0, s[92:95], s62 offen
	v_mov_b32_e32 v95, v1
	v_mov_b32_e32 v96, v1
	s_waitcnt vmcnt(6)
	v_dot8c_i32_i4_e32 v95, v18, v74
	v_dot8c_i32_i4_e32 v96, v18, v70
	v_dot8c_i32_i4_e32 v95, v19, v75
	v_dot8c_i32_i4_e32 v96, v19, v71
	v_dot8c_i32_i4_e32 v95, v20, v76
	v_dot8c_i32_i4_e32 v96, v20, v72
	s_add_i32 s62, s57, -3
	v_dot8c_i32_i4_e32 v95, v21, v77
	v_dot8c_i32_i4_e32 v96, v21, v73
	v_readlane_b32 s62, v83, s62
	s_lshl_b32 s62, s62, 10
	s_nop 0
	v_lshl_add_u32 v18, v95, 4, v96
	v_cvt_f32_i32_e32 v95, v18
	s_nop 0
	buffer_load_dwordx4 v[18:21], v0, s[92:95], s62 offen
	v_mov_b32_e32 v96, v1
	v_mov_b32_e32 v97, v1
	s_waitcnt vmcnt(6)
	v_dot8c_i32_i4_e32 v96, v34, v74
	v_dot8c_i32_i4_e32 v97, v34, v70
	v_dot8c_i32_i4_e32 v96, v35, v75
	v_dot8c_i32_i4_e32 v97, v35, v71
	v_dot8c_i32_i4_e32 v96, v36, v76
	v_dot8c_i32_i4_e32 v97, v36, v72
	s_add_i32 s62, s57, -2
	v_dot8c_i32_i4_e32 v96, v37, v77
	v_dot8c_i32_i4_e32 v97, v37, v73
	v_readlane_b32 s62, v83, s62
	s_lshl_b32 s62, s62, 10
	s_nop 0
	v_lshl_add_u32 v34, v96, 4, v97
	v_cvt_f32_i32_e32 v96, v34
	s_nop 0
	buffer_load_dwordx4 v[34:37], v0, s[92:95], s62 offen
	v_mov_b32_e32 v97, v1
	v_mov_b32_e32 v98, v1
	s_waitcnt vmcnt(6)
	v_dot8c_i32_i4_e32 v97, v50, v74
	v_dot8c_i32_i4_e32 v98, v50, v70
	v_dot8c_i32_i4_e32 v97, v51, v75
	v_dot8c_i32_i4_e32 v98, v51, v71
	v_dot8c_i32_i4_e32 v97, v52, v76
	v_dot8c_i32_i4_e32 v98, v52, v72
	s_add_i32 s62, s57, -1
	v_dot8c_i32_i4_e32 v97, v53, v77
	v_dot8c_i32_i4_e32 v98, v53, v73
	v_readlane_b32 s62, v83, s62
	s_lshl_b32 s62, s62, 10
	s_nop 0
	v_lshl_add_u32 v50, v97, 4, v98
	v_cvt_f32_i32_e32 v97, v50
	s_nop 0
	buffer_load_dwordx4 v[50:53], v0, s[92:95], s62 offen
	v_mov_b32_e32 v98, v1
	v_mov_b32_e32 v99, v1
	s_waitcnt vmcnt(6)
	v_dot8c_i32_i4_e32 v98, v62, v74
	v_dot8c_i32_i4_e32 v99, v62, v70
	v_dot8c_i32_i4_e32 v98, v63, v75
	v_dot8c_i32_i4_e32 v99, v63, v71
	v_readlane_b32 s62, v83, s57
	v_dot8c_i32_i4_e32 v98, v64, v76
	v_dot8c_i32_i4_e32 v99, v64, v72
	s_lshl_b32 s62, s62, 10
	v_dot8c_i32_i4_e32 v98, v65, v77
	v_dot8c_i32_i4_e32 v99, v65, v73
	buffer_load_dwordx4 v[62:65], v0, s[92:95], s62 offen
	s_nop 1
	v_lshl_add_u32 v83, v98, 4, v99
	v_cvt_f32_i32_e32 v83, v83
	v_cndmask_b32_e64 v98, v91, v69, s[0:1]
	v_cndmask_b32_e64 v69, v69, v91, s[0:1]
	v_cndmask_b32_e64 v91, v92, v84, s[0:1]
	v_cndmask_b32_e64 v84, v84, v92, s[0:1]
	v_cndmask_b32_e64 v92, v93, v85, s[0:1]
	v_cndmask_b32_e64 v85, v85, v93, s[0:1]
	v_cndmask_b32_e64 v93, v94, v86, s[0:1]
	v_cndmask_b32_e64 v86, v86, v94, s[0:1]
	v_cndmask_b32_e64 v94, v95, v87, s[0:1]
	v_cndmask_b32_e64 v87, v87, v95, s[0:1]
	v_cndmask_b32_e64 v95, v96, v88, s[0:1]
	v_cndmask_b32_e64 v88, v88, v96, s[0:1]
	v_cndmask_b32_e64 v96, v97, v89, s[0:1]
	v_cndmask_b32_e64 v89, v89, v97, s[0:1]
	v_cndmask_b32_e64 v97, v83, v90, s[0:1]
	v_cndmask_b32_e64 v83, v90, v83, s[0:1]
	ds_bpermute_b32 v69, v190, v69
	ds_bpermute_b32 v84, v190, v84
	ds_bpermute_b32 v85, v190, v85
	ds_bpermute_b32 v86, v190, v86
	ds_bpermute_b32 v87, v190, v87
	ds_bpermute_b32 v88, v190, v88
	ds_bpermute_b32 v89, v190, v89
	ds_bpermute_b32 v83, v190, v83
	s_waitcnt lgkmcnt(7)
	v_add_f32_e32 v69, v98, v69
	s_waitcnt lgkmcnt(6)
	v_add_f32_e32 v84, v91, v84
	s_waitcnt lgkmcnt(5)
	v_add_f32_e32 v85, v92, v85
	s_waitcnt lgkmcnt(4)
	v_add_f32_e32 v86, v93, v86
	s_waitcnt lgkmcnt(3)
	v_add_f32_e32 v87, v94, v87
	s_waitcnt lgkmcnt(2)
	v_add_f32_e32 v88, v95, v88
	s_waitcnt lgkmcnt(1)
	v_add_f32_e32 v89, v96, v89
	s_waitcnt lgkmcnt(0)
	v_add_f32_e32 v83, v97, v83
	v_cndmask_b32_e64 v90, v87, v69, s[2:3]
	v_cndmask_b32_e64 v69, v69, v87, s[2:3]
	v_cndmask_b32_e64 v87, v88, v84, s[2:3]
	v_cndmask_b32_e64 v84, v84, v88, s[2:3]
	v_cndmask_b32_e64 v88, v89, v85, s[2:3]
	v_cndmask_b32_e64 v85, v85, v89, s[2:3]
	v_cndmask_b32_e64 v89, v83, v86, s[2:3]
	v_cndmask_b32_e64 v83, v86, v83, s[2:3]
	ds_bpermute_b32 v69, v189, v69
	ds_bpermute_b32 v84, v189, v84
	ds_bpermute_b32 v85, v189, v85
	ds_bpermute_b32 v83, v189, v83
	s_add_i32 s57, s57, 16
	s_waitcnt lgkmcnt(3)
	v_add_f32_e32 v69, v90, v69
	s_waitcnt lgkmcnt(2)
	v_add_f32_e32 v84, v87, v84
	s_waitcnt lgkmcnt(1)
	v_add_f32_e32 v85, v88, v85
	s_waitcnt lgkmcnt(0)
	v_add_f32_e32 v83, v89, v83
	v_cndmask_b32_e64 v86, v85, v69, s[4:5]
	v_cndmask_b32_e64 v69, v69, v85, s[4:5]
	v_cndmask_b32_e64 v85, v83, v84, s[4:5]
	v_cndmask_b32_e64 v83, v84, v83, s[4:5]
	ds_bpermute_b32 v69, v188, v69
	ds_bpermute_b32 v83, v188, v83
	s_waitcnt lgkmcnt(1)
	v_add_f32_e32 v69, v86, v69
	s_waitcnt lgkmcnt(0)
	v_add_f32_e32 v83, v85, v83
	v_cndmask_b32_e64 v84, v83, v69, s[6:7]
	v_cndmask_b32_e64 v69, v69, v83, s[6:7]
	ds_bpermute_b32 v69, v163, v69
	s_waitcnt lgkmcnt(0)
	v_add_f32_e32 v69, v84, v69
	v_mov_b32_e32 v83, v69
	s_nop 1
	v_permlane16_swap_b32_e32 v69, v83
	v_add_f32_e32 v69, v69, v83
	v_mov_b32_e32 v83, v69
	s_nop 1
	v_permlane32_swap_b32_e32 v69, v83
	v_add_f32_e32 v69, v69, v83
	v_mul_f32_e32 v69, v66, v69
	v_fma_f32 v83, |v69|, s66, 1.0
	v_rcp_f32_e32 v83, v83
	v_mul_f32_e32 v84, v69, v69
	v_mul_f32_e32 v84, 0xbf38aa3b, v84
	v_exp_f32_e32 v84, v84
	v_fmamk_f32 v85, v83, 0x3f07dc22, v207
	v_fmaak_f32 v85, v83, v85, 0x3f35f0e3
	v_fmaak_f32 v85, v83, v85, 0xbe11a98e
	v_fmaak_f32 v85, v83, v85, 0x3e027906
	v_mul_f32_e32 v83, v83, v85
	v_mul_f32_e32 v83, v84, v83
	v_mul_f32_e32 v84, v69, v83
	v_fma_f32 v83, -v69, v83, v69
	v_cmp_gt_f32_e32 vcc, 0, v69
	s_nop 1
	v_cndmask_b32_e32 v69, v83, v84, vcc
	v_mul_f32_e32 v69, 0x3d4ccccd, v69
	v_mul_f32_e32 v69, v82, v69
	v_cmp_eq_u32_e32 vcc, s56, v193
	s_add_i32 s56, s56, 1
	s_cmpk_eq_i32 s57, 0x5f
	v_cndmask_b32_e32 v81, v81, v69, vcc
	s_cbranch_scc0 .LBB0_1419
	s_mov_b32 s56, 0
	v_mov_b32_e32 v82, 0
	s_movk_i32 s57, 0x5f
	s_cmp_eq_u32 s101, 0
	s_cbranch_scc1 .Lnb_1421
	s_barrier
.Lnb_1421:
.LBB0_1421:
	v_mov_b32_e32 v69, v1
	v_mov_b32_e32 v83, v1
	s_waitcnt vmcnt(6)
	v_dot8c_i32_i4_e32 v69, v6, v74
	v_dot8c_i32_i4_e32 v83, v6, v70
	v_dot8c_i32_i4_e32 v69, v7, v75
	v_dot8c_i32_i4_e32 v83, v7, v71
	v_dot8c_i32_i4_e32 v69, v8, v76
	v_dot8c_i32_i4_e32 v83, v8, v72
	s_add_i32 s62, s57, -15
	v_dot8c_i32_i4_e32 v69, v9, v77
	v_dot8c_i32_i4_e32 v83, v9, v73
	s_bitcmp0_b32 s62, 6
	s_cselect_b64 vcc, -1, 0
	s_nop 0
	v_lshl_add_u32 v6, v69, 4, v83
	v_cvt_f32_i32_e32 v69, v6
	v_cndmask_b32_e32 v6, v79, v78, vcc
	s_nop 0
	v_readlane_b32 s62, v6, s62
	s_lshl_b32 s63, s62, 10
	s_cmp_gt_u32 s56, 2
	s_cselect_b32 s62, 0x1000000, 0
	s_add_i32 s63, s63, s62
	buffer_load_dwordx4 v[6:9], v0, s[92:95], s63 offen
	v_mov_b32_e32 v83, v1
	v_mov_b32_e32 v84, v1
	s_waitcnt vmcnt(6)
	v_dot8c_i32_i4_e32 v83, v14, v74
	v_dot8c_i32_i4_e32 v84, v14, v70
	v_dot8c_i32_i4_e32 v83, v15, v75
	v_dot8c_i32_i4_e32 v84, v15, v71
	v_dot8c_i32_i4_e32 v83, v16, v76
	v_dot8c_i32_i4_e32 v84, v16, v72
	s_add_i32 s63, s57, -14
	v_dot8c_i32_i4_e32 v83, v17, v77
	v_dot8c_i32_i4_e32 v84, v17, v73
	s_bitcmp0_b32 s63, 6
	s_cselect_b64 vcc, -1, 0
	s_nop 0
	v_lshl_add_u32 v14, v83, 4, v84
	v_cvt_f32_i32_e32 v83, v14
	v_cndmask_b32_e32 v14, v79, v78, vcc
	s_nop 0
	v_readlane_b32 s63, v14, s63
	s_lshl_b32 s63, s63, 10
	s_add_i32 s63, s63, s62
	s_nop 2
	buffer_load_dwordx4 v[14:17], v0, s[92:95], s63 offen
	v_mov_b32_e32 v84, v1
	v_mov_b32_e32 v85, v1
	s_waitcnt vmcnt(6)
	v_dot8c_i32_i4_e32 v84, v30, v74
	v_dot8c_i32_i4_e32 v85, v30, v70
	v_dot8c_i32_i4_e32 v84, v31, v75
	v_dot8c_i32_i4_e32 v85, v31, v71
	v_dot8c_i32_i4_e32 v84, v32, v76
	v_dot8c_i32_i4_e32 v85, v32, v72
	s_add_i32 s63, s57, -13
	v_dot8c_i32_i4_e32 v84, v33, v77
	v_dot8c_i32_i4_e32 v85, v33, v73
	s_bitcmp0_b32 s63, 6
	s_cselect_b64 vcc, -1, 0
	s_nop 0
	v_lshl_add_u32 v30, v84, 4, v85
	v_cvt_f32_i32_e32 v84, v30
	v_cndmask_b32_e32 v30, v79, v78, vcc
	s_nop 0
	v_readlane_b32 s63, v30, s63
	s_lshl_b32 s63, s63, 10
	s_add_i32 s63, s63, s62
	s_nop 2
	buffer_load_dwordx4 v[30:33], v0, s[92:95], s63 offen
	v_mov_b32_e32 v85, v1
	v_mov_b32_e32 v86, v1
	s_waitcnt vmcnt(6)
	v_dot8c_i32_i4_e32 v85, v46, v74
	v_dot8c_i32_i4_e32 v86, v46, v70
	v_dot8c_i32_i4_e32 v85, v47, v75
	v_dot8c_i32_i4_e32 v86, v47, v71
	v_dot8c_i32_i4_e32 v85, v48, v76
	v_dot8c_i32_i4_e32 v86, v48, v72
	s_add_i32 s63, s57, -12
	v_dot8c_i32_i4_e32 v85, v49, v77
	v_dot8c_i32_i4_e32 v86, v49, v73
	s_bitcmp0_b32 s63, 6
	s_cselect_b64 vcc, -1, 0
	s_nop 0
	v_lshl_add_u32 v46, v85, 4, v86
	v_cvt_f32_i32_e32 v85, v46
	v_cndmask_b32_e32 v46, v79, v78, vcc
	s_nop 0
	v_readlane_b32 s63, v46, s63
	s_lshl_b32 s63, s63, 10
	s_add_i32 s63, s63, s62
	s_nop 2
	buffer_load_dwordx4 v[46:49], v0, s[92:95], s63 offen
	v_mov_b32_e32 v86, v1
	v_mov_b32_e32 v87, v1
	s_waitcnt vmcnt(6)
	v_dot8c_i32_i4_e32 v86, v2, v74
	v_dot8c_i32_i4_e32 v87, v2, v70
	v_dot8c_i32_i4_e32 v86, v3, v75
	v_dot8c_i32_i4_e32 v87, v3, v71
	v_dot8c_i32_i4_e32 v86, v4, v76
	v_dot8c_i32_i4_e32 v87, v4, v72
	s_add_i32 s63, s57, -11
	v_dot8c_i32_i4_e32 v86, v5, v77
	v_dot8c_i32_i4_e32 v87, v5, v73
	s_bitcmp0_b32 s63, 6
	s_cselect_b64 vcc, -1, 0
	s_nop 0
	v_lshl_add_u32 v2, v86, 4, v87
	v_cvt_f32_i32_e32 v86, v2
	v_cndmask_b32_e32 v2, v79, v78, vcc
	s_nop 0
	v_readlane_b32 s63, v2, s63
	s_lshl_b32 s63, s63, 10
	s_add_i32 s63, s63, s62
	s_nop 2
	buffer_load_dwordx4 v[2:5], v0, s[92:95], s63 offen
	v_mov_b32_e32 v87, v1
	v_mov_b32_e32 v88, v1
	s_waitcnt vmcnt(6)
	v_dot8c_i32_i4_e32 v87, v22, v74
	v_dot8c_i32_i4_e32 v88, v22, v70
	v_dot8c_i32_i4_e32 v87, v23, v75
	v_dot8c_i32_i4_e32 v88, v23, v71
	v_dot8c_i32_i4_e32 v87, v24, v76
	v_dot8c_i32_i4_e32 v88, v24, v72
	s_add_i32 s63, s57, -10
	v_dot8c_i32_i4_e32 v87, v25, v77
	v_dot8c_i32_i4_e32 v88, v25, v73
	s_bitcmp0_b32 s63, 6
	s_cselect_b64 vcc, -1, 0
	s_nop 0
	v_lshl_add_u32 v22, v87, 4, v88
	v_cvt_f32_i32_e32 v87, v22
	v_cndmask_b32_e32 v22, v79, v78, vcc
	s_nop 0
	v_readlane_b32 s63, v22, s63
	s_lshl_b32 s63, s63, 10
	s_add_i32 s63, s63, s62
	s_nop 2
	buffer_load_dwordx4 v[22:25], v0, s[92:95], s63 offen
	v_mov_b32_e32 v88, v1
	v_mov_b32_e32 v89, v1
	s_waitcnt vmcnt(6)
	v_dot8c_i32_i4_e32 v88, v38, v74
	v_dot8c_i32_i4_e32 v89, v38, v70
	v_dot8c_i32_i4_e32 v88, v39, v75
	v_dot8c_i32_i4_e32 v89, v39, v71
	v_dot8c_i32_i4_e32 v88, v40, v76
	v_dot8c_i32_i4_e32 v89, v40, v72
	s_add_i32 s63, s57, -9
	v_dot8c_i32_i4_e32 v88, v41, v77
	v_dot8c_i32_i4_e32 v89, v41, v73
	s_bitcmp0_b32 s63, 6
	s_cselect_b64 vcc, -1, 0
	s_nop 0
	v_lshl_add_u32 v38, v88, 4, v89
	v_cvt_f32_i32_e32 v88, v38
	v_cndmask_b32_e32 v38, v79, v78, vcc
	s_nop 0
	v_readlane_b32 s63, v38, s63
	s_lshl_b32 s63, s63, 10
	s_add_i32 s63, s63, s62
	s_nop 2
	buffer_load_dwordx4 v[38:41], v0, s[92:95], s63 offen
	v_mov_b32_e32 v89, v1
	v_mov_b32_e32 v90, v1
	s_waitcnt vmcnt(6)
	v_dot8c_i32_i4_e32 v89, v54, v74
	v_dot8c_i32_i4_e32 v90, v54, v70
	v_dot8c_i32_i4_e32 v89, v55, v75
	v_dot8c_i32_i4_e32 v90, v55, v71
	v_dot8c_i32_i4_e32 v89, v56, v76
	v_dot8c_i32_i4_e32 v90, v56, v72
	s_add_i32 s63, s57, -8
	v_dot8c_i32_i4_e32 v89, v57, v77
	v_dot8c_i32_i4_e32 v90, v57, v73
	s_bitcmp0_b32 s63, 6
	s_cselect_b64 vcc, -1, 0
	s_nop 0
	v_lshl_add_u32 v54, v89, 4, v90
	v_cvt_f32_i32_e32 v89, v54
	v_cndmask_b32_e32 v54, v79, v78, vcc
	s_nop 0
	v_readlane_b32 s63, v54, s63
	s_lshl_b32 s63, s63, 10
	s_add_i32 s63, s63, s62
	s_nop 2
	buffer_load_dwordx4 v[54:57], v0, s[92:95], s63 offen
	v_mov_b32_e32 v90, v1
	v_mov_b32_e32 v91, v1
	s_waitcnt vmcnt(6)
	v_dot8c_i32_i4_e32 v90, v10, v74
	v_dot8c_i32_i4_e32 v91, v10, v70
	v_dot8c_i32_i4_e32 v90, v11, v75
	v_dot8c_i32_i4_e32 v91, v11, v71
	v_dot8c_i32_i4_e32 v90, v12, v76
	v_dot8c_i32_i4_e32 v91, v12, v72
	s_add_i32 s63, s57, -7
	v_dot8c_i32_i4_e32 v90, v13, v77
	v_dot8c_i32_i4_e32 v91, v13, v73
	s_bitcmp0_b32 s63, 6
	s_cselect_b64 vcc, -1, 0
	s_nop 0
	v_lshl_add_u32 v10, v90, 4, v91
	v_cvt_f32_i32_e32 v90, v10
	v_cndmask_b32_e32 v10, v79, v78, vcc
	s_nop 0
	v_readlane_b32 s63, v10, s63
	s_lshl_b32 s63, s63, 10
	s_add_i32 s63, s63, s62
	s_nop 2
	buffer_load_dwordx4 v[10:13], v0, s[92:95], s63 offen
	v_mov_b32_e32 v91, v1
	v_mov_b32_e32 v92, v1
	s_waitcnt vmcnt(6)
	v_dot8c_i32_i4_e32 v91, v26, v74
	v_dot8c_i32_i4_e32 v92, v26, v70
	v_dot8c_i32_i4_e32 v91, v27, v75
	v_dot8c_i32_i4_e32 v92, v27, v71
	v_dot8c_i32_i4_e32 v91, v28, v76
	v_dot8c_i32_i4_e32 v92, v28, v72
	s_add_i32 s63, s57, -6
	v_dot8c_i32_i4_e32 v91, v29, v77
	v_dot8c_i32_i4_e32 v92, v29, v73
	s_bitcmp0_b32 s63, 6
	s_cselect_b64 vcc, -1, 0
	s_nop 0
	v_lshl_add_u32 v26, v91, 4, v92
	v_cvt_f32_i32_e32 v91, v26
	v_cndmask_b32_e32 v26, v79, v78, vcc
	s_nop 0
	v_readlane_b32 s63, v26, s63
	s_lshl_b32 s63, s63, 10
	s_add_i32 s63, s63, s62
	s_nop 2
	buffer_load_dwordx4 v[26:29], v0, s[92:95], s63 offen
	v_mov_b32_e32 v92, v1
	v_mov_b32_e32 v93, v1
	s_waitcnt vmcnt(6)
	v_dot8c_i32_i4_e32 v92, v42, v74
	v_dot8c_i32_i4_e32 v93, v42, v70
	v_dot8c_i32_i4_e32 v92, v43, v75
	v_dot8c_i32_i4_e32 v93, v43, v71
	v_dot8c_i32_i4_e32 v92, v44, v76
	v_dot8c_i32_i4_e32 v93, v44, v72
	s_add_i32 s63, s57, -5
	v_dot8c_i32_i4_e32 v92, v45, v77
	v_dot8c_i32_i4_e32 v93, v45, v73
	s_bitcmp0_b32 s63, 6
	s_cselect_b64 vcc, -1, 0
	s_nop 0
	v_lshl_add_u32 v42, v92, 4, v93
	v_cvt_f32_i32_e32 v92, v42
	v_cndmask_b32_e32 v42, v79, v78, vcc
	s_nop 0
	v_readlane_b32 s63, v42, s63
	s_lshl_b32 s63, s63, 10
	s_add_i32 s63, s63, s62
	s_nop 2
	buffer_load_dwordx4 v[42:45], v0, s[92:95], s63 offen
	v_mov_b32_e32 v93, v1
	v_mov_b32_e32 v94, v1
	s_waitcnt vmcnt(6)
	v_dot8c_i32_i4_e32 v93, v58, v74
	v_dot8c_i32_i4_e32 v94, v58, v70
	v_dot8c_i32_i4_e32 v93, v59, v75
	v_dot8c_i32_i4_e32 v94, v59, v71
	v_dot8c_i32_i4_e32 v93, v60, v76
	v_dot8c_i32_i4_e32 v94, v60, v72
	s_add_i32 s63, s57, -4
	v_dot8c_i32_i4_e32 v93, v61, v77
	v_dot8c_i32_i4_e32 v94, v61, v73
	s_bitcmp0_b32 s63, 6
	s_cselect_b64 vcc, -1, 0
	s_nop 0
	v_lshl_add_u32 v58, v93, 4, v94
	v_cvt_f32_i32_e32 v93, v58
	v_cndmask_b32_e32 v58, v79, v78, vcc
	s_nop 0
	v_readlane_b32 s63, v58, s63
	s_lshl_b32 s63, s63, 10
	s_add_i32 s63, s63, s62
	s_nop 2
	buffer_load_dwordx4 v[58:61], v0, s[92:95], s63 offen
	v_mov_b32_e32 v94, v1
	v_mov_b32_e32 v95, v1
	s_waitcnt vmcnt(6)
	v_dot8c_i32_i4_e32 v94, v18, v74
	v_dot8c_i32_i4_e32 v95, v18, v70
	v_dot8c_i32_i4_e32 v94, v19, v75
	v_dot8c_i32_i4_e32 v95, v19, v71
	v_dot8c_i32_i4_e32 v94, v20, v76
	v_dot8c_i32_i4_e32 v95, v20, v72
	s_add_i32 s63, s57, -3
	v_dot8c_i32_i4_e32 v94, v21, v77
	v_dot8c_i32_i4_e32 v95, v21, v73
	s_bitcmp0_b32 s63, 6
	s_cselect_b64 vcc, -1, 0
	s_nop 0
	v_lshl_add_u32 v18, v94, 4, v95
	v_cvt_f32_i32_e32 v94, v18
	v_cndmask_b32_e32 v18, v79, v78, vcc
	s_nop 0
	v_readlane_b32 s63, v18, s63
	s_lshl_b32 s63, s63, 10
	s_add_i32 s63, s63, s62
	s_nop 2
	buffer_load_dwordx4 v[18:21], v0, s[92:95], s63 offen
	v_mov_b32_e32 v95, v1
	v_mov_b32_e32 v96, v1
	s_waitcnt vmcnt(6)
	v_dot8c_i32_i4_e32 v95, v34, v74
	v_dot8c_i32_i4_e32 v96, v34, v70
	v_dot8c_i32_i4_e32 v95, v35, v75
	v_dot8c_i32_i4_e32 v96, v35, v71
	v_dot8c_i32_i4_e32 v95, v36, v76
	v_dot8c_i32_i4_e32 v96, v36, v72
	s_add_i32 s63, s57, -2
	v_dot8c_i32_i4_e32 v95, v37, v77
	v_dot8c_i32_i4_e32 v96, v37, v73
	s_bitcmp0_b32 s63, 6
	s_cselect_b64 vcc, -1, 0
	s_nop 0
	v_lshl_add_u32 v34, v95, 4, v96
	v_cvt_f32_i32_e32 v95, v34
	v_cndmask_b32_e32 v34, v79, v78, vcc
	s_nop 0
	v_readlane_b32 s63, v34, s63
	s_lshl_b32 s63, s63, 10
	s_add_i32 s63, s63, s62
	s_nop 2
	buffer_load_dwordx4 v[34:37], v0, s[92:95], s63 offen
	v_mov_b32_e32 v96, v1
	v_mov_b32_e32 v97, v1
	s_waitcnt vmcnt(6)
	v_dot8c_i32_i4_e32 v96, v50, v74
	v_dot8c_i32_i4_e32 v97, v50, v70
	v_dot8c_i32_i4_e32 v96, v51, v75
	v_dot8c_i32_i4_e32 v97, v51, v71
	v_dot8c_i32_i4_e32 v96, v52, v76
	v_dot8c_i32_i4_e32 v97, v52, v72
	s_add_i32 s63, s57, -1
	v_dot8c_i32_i4_e32 v96, v53, v77
	v_dot8c_i32_i4_e32 v97, v53, v73
	s_bitcmp0_b32 s63, 6
	s_cselect_b64 vcc, -1, 0
	s_nop 0
	v_lshl_add_u32 v50, v96, 4, v97
	v_cvt_f32_i32_e32 v96, v50
	v_cndmask_b32_e32 v50, v79, v78, vcc
	s_nop 0
	v_readlane_b32 s63, v50, s63
	s_lshl_b32 s63, s63, 10
	s_add_i32 s63, s63, s62
	s_nop 2
	buffer_load_dwordx4 v[50:53], v0, s[92:95], s63 offen
	v_mov_b32_e32 v97, v1
	v_mov_b32_e32 v98, v1
	s_waitcnt vmcnt(6)
	v_dot8c_i32_i4_e32 v97, v62, v74
	v_dot8c_i32_i4_e32 v98, v62, v70
	v_dot8c_i32_i4_e32 v97, v63, v75
	v_dot8c_i32_i4_e32 v98, v63, v71
	v_dot8c_i32_i4_e32 v97, v64, v76
	v_dot8c_i32_i4_e32 v98, v64, v72
	v_dot8c_i32_i4_e32 v97, v65, v77
	v_dot8c_i32_i4_e32 v98, v65, v73
	s_bitcmp0_b32 s57, 6
	s_cselect_b64 vcc, -1, 0
	s_nop 0
	v_lshl_add_u32 v62, v97, 4, v98
	v_cvt_f32_i32_e32 v97, v62
	v_cndmask_b32_e32 v62, v79, v78, vcc
	s_nop 0
	v_readlane_b32 s63, v62, s57
	s_lshl_b32 s63, s63, 10
	s_add_i32 s63, s63, s62
	s_nop 2
	buffer_load_dwordx4 v[62:65], v0, s[92:95], s63 offen
	v_cndmask_b32_e64 v98, v90, v69, s[0:1]
	v_cndmask_b32_e64 v69, v69, v90, s[0:1]
	v_cndmask_b32_e64 v90, v91, v83, s[0:1]
	v_cndmask_b32_e64 v83, v83, v91, s[0:1]
	v_cndmask_b32_e64 v91, v92, v84, s[0:1]
	v_cndmask_b32_e64 v84, v84, v92, s[0:1]
	v_cndmask_b32_e64 v92, v93, v85, s[0:1]
	v_cndmask_b32_e64 v85, v85, v93, s[0:1]
	v_cndmask_b32_e64 v93, v94, v86, s[0:1]
	v_cndmask_b32_e64 v86, v86, v94, s[0:1]
	v_cndmask_b32_e64 v94, v95, v87, s[0:1]
	v_cndmask_b32_e64 v87, v87, v95, s[0:1]
	v_cndmask_b32_e64 v95, v96, v88, s[0:1]
	v_cndmask_b32_e64 v88, v88, v96, s[0:1]
	v_cndmask_b32_e64 v96, v97, v89, s[0:1]
	v_cndmask_b32_e64 v89, v89, v97, s[0:1]
	ds_bpermute_b32 v69, v190, v69
	ds_bpermute_b32 v83, v190, v83
	ds_bpermute_b32 v84, v190, v84
	ds_bpermute_b32 v85, v190, v85
	ds_bpermute_b32 v86, v190, v86
	ds_bpermute_b32 v87, v190, v87
	ds_bpermute_b32 v88, v190, v88
	ds_bpermute_b32 v89, v190, v89
	s_waitcnt lgkmcnt(7)
; __device__ __forceinline__ int shl_i(int v, int from_lane) { return __builtin_amdgcn_ds_bpermute(from_lane << 2, v); }
;     ...
;         GATHER_U_SECTION(0, g0, w0)
;         GATHER_U_SECTION(1, g1, w1)
;         const float wm = wave_max(fmaxf(fabsf(w0), fabsf(w1)));
;         const float wsq = (wm > 0.f) ? 127.0f / wm : 0.f;
;         const int q0 = (int)rintf(w0 * wsq), q1 = (int)rintf(w1 * wsq);
;         const int c8 = 8 * (int)wave_sum((float)(q0 + q1));
;         const int pk0 = (q0 & 0xFF) | ((shl_i(q0, lane + 1) & 0xFF) << 8) | ((shl_i(q0, lane + 2) & 0xFF) << 16) | (shl_i(q0, lane + 3) << 24);
;         const int pk1 = (q1 & 0xFF) | ((shl_i(q1, lane + 1) & 0xFF) << 8) | ((shl_i(q1, lane + 2) & 0xFF) << 16) | (shl_i(q1, lane + 3) << 24);
;         int acci[32];
; #pragma unroll
;         for (int i = 0; i < 32; ++i) acci[i] = 0;
	v_add_f32_e32 v69, v98, v69
	s_waitcnt lgkmcnt(6)
	v_add_f32_e32 v83, v90, v83
	s_waitcnt lgkmcnt(5)
	v_add_f32_e32 v84, v91, v84
	s_waitcnt lgkmcnt(4)
	v_add_f32_e32 v85, v92, v85
	s_waitcnt lgkmcnt(3)
	v_add_f32_e32 v86, v93, v86
	s_waitcnt lgkmcnt(2)
	v_add_f32_e32 v87, v94, v87
	s_waitcnt lgkmcnt(1)
	v_add_f32_e32 v88, v95, v88
	s_waitcnt lgkmcnt(0)
	v_add_f32_e32 v89, v96, v89
	v_cndmask_b32_e64 v90, v86, v69, s[2:3]
	v_cndmask_b32_e64 v69, v69, v86, s[2:3]
	v_cndmask_b32_e64 v86, v87, v83, s[2:3]
	v_cndmask_b32_e64 v83, v83, v87, s[2:3]
	v_cndmask_b32_e64 v87, v88, v84, s[2:3]
	v_cndmask_b32_e64 v84, v84, v88, s[2:3]
	v_cndmask_b32_e64 v88, v89, v85, s[2:3]
	v_cndmask_b32_e64 v85, v85, v89, s[2:3]
	ds_bpermute_b32 v69, v189, v69
	ds_bpermute_b32 v83, v189, v83
	ds_bpermute_b32 v84, v189, v84
	ds_bpermute_b32 v85, v189, v85
	s_add_i32 s57, s57, 16
	s_waitcnt lgkmcnt(3)
	v_add_f32_e32 v69, v90, v69
	s_waitcnt lgkmcnt(2)
	v_add_f32_e32 v83, v86, v83
	s_waitcnt lgkmcnt(1)
	v_add_f32_e32 v84, v87, v84
	s_waitcnt lgkmcnt(0)
	v_add_f32_e32 v85, v88, v85
	v_cndmask_b32_e64 v86, v84, v69, s[4:5]
	v_cndmask_b32_e64 v69, v69, v84, s[4:5]
	v_cndmask_b32_e64 v84, v85, v83, s[4:5]
	v_cndmask_b32_e64 v83, v83, v85, s[4:5]
	ds_bpermute_b32 v69, v188, v69
	ds_bpermute_b32 v83, v188, v83
	s_waitcnt lgkmcnt(1)
	v_add_f32_e32 v69, v86, v69
	s_waitcnt lgkmcnt(0)
	v_add_f32_e32 v83, v84, v83
	v_cndmask_b32_e64 v84, v83, v69, s[6:7]
	v_cndmask_b32_e64 v69, v69, v83, s[6:7]
	ds_bpermute_b32 v69, v163, v69
	s_waitcnt lgkmcnt(0)
	v_add_f32_e32 v69, v84, v69
	v_mov_b32_e32 v83, v69
	s_nop 1
	v_permlane16_swap_b32_e32 v69, v83
	v_add_f32_e32 v69, v69, v83
	v_mov_b32_e32 v83, v69
	s_nop 1
	v_permlane32_swap_b32_e32 v69, v83
	v_add_f32_e32 v69, v69, v83
	v_mul_f32_e32 v69, v66, v69
	v_fma_f32 v83, |v69|, s66, 1.0
	v_rcp_f32_e32 v83, v83
	v_mul_f32_e32 v84, v69, v69
	v_mul_f32_e32 v84, 0xbf38aa3b, v84
	v_exp_f32_e32 v84, v84
	v_fmamk_f32 v85, v83, 0x3f07dc22, v207
	v_fmaak_f32 v85, v83, v85, 0x3f35f0e3
	v_fmaak_f32 v85, v83, v85, 0xbe11a98e
	v_fmaak_f32 v85, v83, v85, 0x3e027906
	v_mul_f32_e32 v83, v83, v85
	v_mul_f32_e32 v83, v84, v83
	v_mul_f32_e32 v84, v69, v83
	v_fma_f32 v83, -v69, v83, v69
	v_cmp_gt_f32_e32 vcc, 0, v69
	s_nop 1
	v_cndmask_b32_e32 v69, v83, v84, vcc
	v_mul_f32_e32 v69, 0x3d4ccccd, v69
	v_mul_f32_e32 v69, v80, v69
	v_cmp_eq_u32_e32 vcc, s56, v193
	s_add_i32 s56, s56, 1
	s_cmpk_eq_i32 s57, 0x9f
	v_cndmask_b32_e32 v82, v82, v69, vcc
	s_cbranch_scc0 .LBB0_1421
	v_max_f32_e64 v66, |v82|, |v82|
	v_max_f32_e64 v69, |v81|, |v81|
	v_max_f32_e32 v66, v69, v66
	v_mov_b32_e32 v69, 0
	s_mov_b32 s57, 0x42fe0000
	v_mbcnt_lo_u32_b32 v69, -1, v69
	v_mbcnt_hi_u32_b32 v69, -1, v69
	v_lshlrev_b32_e32 v71, 2, v69
	v_xor_b32_e32 v69, 0x80, v71
	ds_bpermute_b32 v69, v69, v66
	v_xor_b32_e32 v70, 64, v71
	v_xor_b32_e32 v72, 8, v71
	v_mov_b32_e32 v83, 0
	s_waitcnt lgkmcnt(0)
	v_max_f32_e32 v69, v69, v69
	v_max_f32_e32 v66, v66, v69
	ds_bpermute_b32 v69, v70, v66
	v_xor_b32_e32 v70, 32, v71
	s_movk_i32 s56, 0x9f
	v_mov_b32_e32 v74, 0
	v_mov_b32_e32 v75, 0
	s_waitcnt lgkmcnt(0)
	v_max_f32_e32 v69, v69, v69
	v_max_f32_e32 v66, v66, v69
	ds_bpermute_b32 v69, v70, v66
	v_xor_b32_e32 v70, 16, v71
	v_xor_b32_e32 v71, 4, v71
	v_mov_b32_e32 v76, 0
	v_mov_b32_e32 v80, 0
	s_waitcnt lgkmcnt(0)
	v_max_f32_e32 v69, v69, v69
	v_max_f32_e32 v69, v66, v69
	ds_bpermute_b32 v70, v70, v69
	v_mov_b32_e32 v66, 0
	v_mov_b32_e32 v94, 0
	v_mov_b32_e32 v95, 0
	v_mov_b32_e32 v96, 0
	s_waitcnt lgkmcnt(0)
	v_max_f32_e32 v70, v70, v70
	v_max_f32_e32 v73, v69, v70
	ds_bpermute_b32 v72, v72, v73
	v_mov_b32_e32 v69, 0
	v_mov_b32_e32 v70, 0
	v_mov_b32_e32 v97, 0
	v_mov_b32_e32 v98, 0
	s_waitcnt lgkmcnt(0)
	v_max_f32_e32 v72, v72, v72
	v_max_f32_e32 v77, v73, v72
	ds_bpermute_b32 v71, v71, v77
	v_mov_b32_e32 v72, 0
	v_mov_b32_e32 v73, 0
	v_mov_b32_e32 v99, 0
	v_mov_b32_e32 v100, 0
	s_waitcnt lgkmcnt(0)
	v_max_f32_e32 v71, v71, v71
	v_max_f32_e32 v71, v77, v71
	v_div_scale_f32 v77, s[62:63], v71, v71, s57
	v_rcp_f32_e32 v84, v77
	v_div_scale_f32 v85, vcc, s57, v71, s57
	v_mov_b32_e32 v101, 0
	v_fma_f32 v86, -v77, v84, 1.0
	v_fmac_f32_e32 v84, v86, v84
	v_mul_f32_e32 v86, v85, v84
	v_fma_f32 v87, -v77, v86, v85
	v_fmac_f32_e32 v86, v87, v84
	v_fma_f32 v77, -v77, v86, v85
	v_div_fmas_f32 v77, v77, v84, v86
	v_div_fixup_f32 v77, v77, v71, s57
	v_cmp_lt_f32_e32 vcc, 0, v71
	s_mov_b32 s57, 0xc0c0500
	v_mov_b32_e32 v85, 0
	v_cndmask_b32_e32 v77, 0, v77, vcc
	v_mul_f32_e32 v81, v81, v77
	v_mul_f32_e32 v77, v82, v77
	v_rndne_f32_e32 v81, v81
	v_rndne_f32_e32 v77, v77
	v_cvt_i32_f32_e32 v82, v81
	v_cvt_i32_f32_e32 v107, v77
	v_mbcnt_lo_u32_b32 v81, -1, v83
	v_mbcnt_hi_u32_b32 v81, -1, v81
	v_lshlrev_b32_e32 v84, 2, v81
	v_add_u32_e32 v83, v82, v107
	v_cvt_f32_i32_e32 v83, v83
	v_xor_b32_e32 v81, 0x80, v84
	v_xor_b32_e32 v88, 64, v84
	v_xor_b32_e32 v89, 16, v84
	ds_bpermute_b32 v87, v81, v83
	v_xor_b32_e32 v90, 8, v84
	ds_bpermute_b32 v91, v195, v82
	ds_bpermute_b32 v92, v196, v82
	ds_bpermute_b32 v108, v194, v107
	s_waitcnt lgkmcnt(3)
	v_add_f32_e32 v83, v87, v83
	ds_bpermute_b32 v87, v88, v83
	v_xor_b32_e32 v88, 32, v84
	v_xor_b32_e32 v84, 4, v84
	ds_bpermute_b32 v109, v195, v107
	ds_bpermute_b32 v110, v196, v107
	s_waitcnt lgkmcnt(2)
	v_add_f32_e32 v83, v83, v87
	ds_bpermute_b32 v87, v88, v83
	ds_bpermute_b32 v88, v194, v82
	v_mov_b32_e32 v77, 0
	v_mov_b32_e32 v81, 0
	v_mov_b32_e32 v86, 0
	s_waitcnt lgkmcnt(1)
	v_add_f32_e32 v83, v83, v87
	ds_bpermute_b32 v87, v89, v83
	s_waitcnt lgkmcnt(1)
	v_lshlrev_b32_e32 v88, 8, v88
	v_lshlrev_b32_e32 v89, 16, v91
	v_perm_b32 v82, v88, v82, s57
	v_and_b32_e32 v88, 0xff0000, v89
	s_waitcnt lgkmcnt(0)
	v_add_f32_e32 v83, v83, v87
	ds_bpermute_b32 v87, v90, v83
	v_lshlrev_b32_e32 v90, 24, v92
	v_or3_b32 v111, v82, v88, v90
	v_mov_b32_e32 v82, 0
	v_mov_b32_e32 v88, 0
	s_waitcnt lgkmcnt(0)
	v_add_f32_e32 v103, v83, v87
	ds_bpermute_b32 v104, v84, v103
	v_mov_b32_e32 v84, 0
	v_mov_b32_e32 v87, 0
	v_mov_b32_e32 v89, 0
	v_mov_b32_e32 v90, 0
	v_mov_b32_e32 v91, 0
	v_mov_b32_e32 v92, 0
	v_mov_b32_e32 v93, 0
	v_mov_b32_e32 v102, 0
	v_mov_b32_e32 v83, 0
	s_cmp_eq_u32 s101, 0
	s_cbranch_scc1 .Lnb_1423
	s_barrier
.Lnb_1423:
.LBB0_1423:
	s_add_i32 s57, s56, 0xffffff61
	s_waitcnt vmcnt(5)
	v_perm_b32 v112, v14, v6, s67
	v_perm_b32 v6, v14, v6, s68
	s_waitcnt vmcnt(3)
	v_perm_b32 v14, v46, v30, s67
	v_readlane_b32 s57, v111, s57
	v_perm_b32 v30, v46, v30, s68
	v_perm_b32 v46, v14, v112, s69
	v_perm_b32 v14, v14, v112, s33
	v_perm_b32 v112, v30, v6, s69
	v_perm_b32 v6, v30, v6, s33
	v_dot4c_i32_i8_e32 v74, s57, v14
	v_and_b32_e32 v14, 0xf0f0f0f0, v14
	v_dot4c_i32_i8_e32 v70, s57, v14
	v_and_b32_e32 v14, 0xf0f0f0f0, v112
	v_dot4c_i32_i8_e32 v76, s57, v6
	v_and_b32_e32 v6, 0xf0f0f0f0, v6
	v_and_b32_e32 v30, 0xf0f0f0f0, v46
	v_dot4c_i32_i8_e32 v72, s57, v14
	v_dot4c_i32_i8_e32 v73, s57, v6
	v_perm_b32 v6, v15, v7, s67
	v_perm_b32 v14, v47, v31, s67
	v_dot4c_i32_i8_e32 v69, s57, v30
	v_perm_b32 v7, v15, v7, s68
	v_perm_b32 v15, v47, v31, s68
	v_perm_b32 v30, v14, v6, s69
	v_perm_b32 v6, v14, v6, s33
	v_perm_b32 v14, v15, v7, s69
	v_dot4c_i32_i8_e32 v85, s57, v6
	v_and_b32_e32 v6, 0xf0f0f0f0, v6
	v_perm_b32 v7, v15, v7, s33
	v_dot4c_i32_i8_e32 v81, s57, v6
	v_and_b32_e32 v6, 0xf0f0f0f0, v14
	v_dot4c_i32_i8_e32 v82, s57, v6
	v_and_b32_e32 v6, 0xf0f0f0f0, v7
	v_and_b32_e32 v15, 0xf0f0f0f0, v30
	v_dot4c_i32_i8_e32 v94, s57, v7
	v_dot4c_i32_i8_e32 v84, s57, v6
	v_perm_b32 v6, v16, v8, s67
	v_perm_b32 v7, v16, v8, s68
	v_perm_b32 v8, v48, v32, s67
	v_dot4c_i32_i8_e32 v77, s57, v15
	v_dot4c_i32_i8_e32 v86, s57, v14
	v_perm_b32 v14, v48, v32, s68
	v_perm_b32 v15, v8, v6, s69
	v_perm_b32 v6, v8, v6, s33
	v_perm_b32 v8, v14, v7, s69
	v_dot4c_i32_i8_e32 v96, s57, v6
	v_and_b32_e32 v6, 0xf0f0f0f0, v6
	v_perm_b32 v7, v14, v7, s33
	v_dot4c_i32_i8_e32 v88, s57, v6
	v_and_b32_e32 v6, 0xf0f0f0f0, v8
	v_dot4c_i32_i8_e32 v89, s57, v6
	v_and_b32_e32 v6, 0xf0f0f0f0, v7
	v_and_b32_e32 v14, 0xf0f0f0f0, v15
	v_dot4c_i32_i8_e32 v97, s57, v8
	v_dot4c_i32_i8_e32 v90, s57, v6
	v_perm_b32 v6, v17, v9, s67
	v_perm_b32 v8, v49, v33, s67
	v_dot4c_i32_i8_e32 v87, s57, v14
	v_dot4c_i32_i8_e32 v98, s57, v7
	v_perm_b32 v7, v17, v9, s68
	v_perm_b32 v9, v49, v33, s68
	v_perm_b32 v14, v8, v6, s69
	v_perm_b32 v6, v8, v6, s33
	v_perm_b32 v8, v9, v7, s69
	v_dot4c_i32_i8_e32 v100, s57, v6
	v_and_b32_e32 v6, 0xf0f0f0f0, v6
	v_perm_b32 v7, v9, v7, s33
	v_dot4c_i32_i8_e32 v92, s57, v6
	v_and_b32_e32 v6, 0xf0f0f0f0, v8
	v_and_b32_e32 v9, 0xf0f0f0f0, v14
	v_dot4c_i32_i8_e32 v93, s57, v6
	v_and_b32_e32 v6, 0xf0f0f0f0, v7
	v_dot4c_i32_i8_e32 v66, s57, v46
	v_dot4c_i32_i8_e32 v75, s57, v112
	v_dot4c_i32_i8_e32 v80, s57, v30
	v_dot4c_i32_i8_e32 v95, s57, v15
	v_dot4c_i32_i8_e32 v99, s57, v14
	v_dot4c_i32_i8_e32 v91, s57, v9
	v_dot4c_i32_i8_e32 v101, s57, v8
	v_dot4c_i32_i8_e32 v102, s57, v7
	v_dot4c_i32_i8_e32 v83, s57, v6
	s_add_i32 s57, s56, -15
	s_bitcmp0_b32 s57, 6
	s_cselect_b64 vcc, -1, 0
	v_cndmask_b32_e32 v6, v79, v78, vcc
	s_nop 0
	v_readlane_b32 s57, v6, s57
	s_lshl_b32 s57, s57, 10
	s_add_i32 s57, s57, 0x1000000
	s_nop 2
	buffer_load_dwordx4 v[6:9], v0, s[92:95], s57 offen
	s_add_i32 s57, s56, -14
	s_bitcmp0_b32 s57, 6
	s_cselect_b64 vcc, -1, 0
	v_cndmask_b32_e32 v14, v79, v78, vcc
	s_nop 0
	v_readlane_b32 s57, v14, s57
	s_lshl_b32 s57, s57, 10
	s_add_i32 s57, s57, 0x1000000
	s_nop 2
	buffer_load_dwordx4 v[14:17], v0, s[92:95], s57 offen
	s_add_i32 s57, s56, -13
	s_bitcmp0_b32 s57, 6
	s_cselect_b64 vcc, -1, 0
	v_cndmask_b32_e32 v30, v79, v78, vcc
	s_nop 0
	v_readlane_b32 s57, v30, s57
	s_lshl_b32 s57, s57, 10
	s_add_i32 s57, s57, 0x1000000
	s_nop 2
	buffer_load_dwordx4 v[30:33], v0, s[92:95], s57 offen
	s_add_i32 s57, s56, -12
	s_bitcmp0_b32 s57, 6
	s_cselect_b64 vcc, -1, 0
	v_cndmask_b32_e32 v46, v79, v78, vcc
	s_nop 0
	v_readlane_b32 s57, v46, s57
	s_lshl_b32 s57, s57, 10
	s_add_i32 s57, s57, 0x1000000
	s_nop 2
	buffer_load_dwordx4 v[46:49], v0, s[92:95], s57 offen
	s_add_i32 s57, s56, 0xffffff65
	s_waitcnt vmcnt(5)
	v_perm_b32 v112, v22, v2, s67
	v_perm_b32 v2, v22, v2, s68
	s_waitcnt vmcnt(3)
	v_perm_b32 v22, v54, v38, s67
	v_readlane_b32 s57, v111, s57
	v_perm_b32 v38, v54, v38, s68
	v_perm_b32 v54, v22, v112, s69
	v_perm_b32 v22, v22, v112, s33
	v_perm_b32 v112, v38, v2, s69
	v_perm_b32 v2, v38, v2, s33
	v_dot4c_i32_i8_e32 v74, s57, v22
	v_and_b32_e32 v22, 0xf0f0f0f0, v22
	v_dot4c_i32_i8_e32 v70, s57, v22
	v_and_b32_e32 v22, 0xf0f0f0f0, v112
	v_dot4c_i32_i8_e32 v76, s57, v2
	v_and_b32_e32 v2, 0xf0f0f0f0, v2
	v_and_b32_e32 v38, 0xf0f0f0f0, v54
	v_dot4c_i32_i8_e32 v72, s57, v22
	v_dot4c_i32_i8_e32 v73, s57, v2
	v_perm_b32 v2, v23, v3, s67
	v_perm_b32 v22, v55, v39, s67
	v_dot4c_i32_i8_e32 v69, s57, v38
	v_perm_b32 v3, v23, v3, s68
	v_perm_b32 v23, v55, v39, s68
	v_perm_b32 v38, v22, v2, s69
	v_perm_b32 v2, v22, v2, s33
	v_perm_b32 v22, v23, v3, s69
	v_dot4c_i32_i8_e32 v85, s57, v2
	v_and_b32_e32 v2, 0xf0f0f0f0, v2
	v_perm_b32 v3, v23, v3, s33
	v_dot4c_i32_i8_e32 v81, s57, v2
	v_and_b32_e32 v2, 0xf0f0f0f0, v22
	v_dot4c_i32_i8_e32 v82, s57, v2
	v_and_b32_e32 v2, 0xf0f0f0f0, v3
	v_and_b32_e32 v23, 0xf0f0f0f0, v38
	v_dot4c_i32_i8_e32 v94, s57, v3
	v_dot4c_i32_i8_e32 v84, s57, v2
	v_perm_b32 v2, v24, v4, s67
	v_perm_b32 v3, v24, v4, s68
	v_perm_b32 v4, v56, v40, s67
	v_dot4c_i32_i8_e32 v77, s57, v23
	v_dot4c_i32_i8_e32 v86, s57, v22
	v_perm_b32 v22, v56, v40, s68
	v_perm_b32 v23, v4, v2, s69
	v_perm_b32 v2, v4, v2, s33
	v_perm_b32 v4, v22, v3, s69
	v_dot4c_i32_i8_e32 v96, s57, v2
	v_and_b32_e32 v2, 0xf0f0f0f0, v2
	v_perm_b32 v3, v22, v3, s33
	v_dot4c_i32_i8_e32 v88, s57, v2
	v_and_b32_e32 v2, 0xf0f0f0f0, v4
	v_dot4c_i32_i8_e32 v89, s57, v2
	v_and_b32_e32 v2, 0xf0f0f0f0, v3
	v_and_b32_e32 v22, 0xf0f0f0f0, v23
	v_dot4c_i32_i8_e32 v97, s57, v4
	v_dot4c_i32_i8_e32 v90, s57, v2
	v_perm_b32 v2, v25, v5, s67
	v_perm_b32 v4, v57, v41, s67
	v_dot4c_i32_i8_e32 v87, s57, v22
	v_dot4c_i32_i8_e32 v98, s57, v3
	v_perm_b32 v3, v25, v5, s68
	v_perm_b32 v5, v57, v41, s68
	v_perm_b32 v22, v4, v2, s69
	v_perm_b32 v2, v4, v2, s33
	v_perm_b32 v4, v5, v3, s69
	v_dot4c_i32_i8_e32 v100, s57, v2
	v_and_b32_e32 v2, 0xf0f0f0f0, v2
	v_perm_b32 v3, v5, v3, s33
	v_dot4c_i32_i8_e32 v92, s57, v2
	v_and_b32_e32 v2, 0xf0f0f0f0, v4
	v_and_b32_e32 v5, 0xf0f0f0f0, v22
	v_dot4c_i32_i8_e32 v93, s57, v2
	v_and_b32_e32 v2, 0xf0f0f0f0, v3
	v_dot4c_i32_i8_e32 v66, s57, v54
	v_dot4c_i32_i8_e32 v75, s57, v112
	v_dot4c_i32_i8_e32 v80, s57, v38
	v_dot4c_i32_i8_e32 v95, s57, v23
	v_dot4c_i32_i8_e32 v99, s57, v22
	v_dot4c_i32_i8_e32 v91, s57, v5
	v_dot4c_i32_i8_e32 v101, s57, v4
	v_dot4c_i32_i8_e32 v102, s57, v3
	v_dot4c_i32_i8_e32 v83, s57, v2
	s_add_i32 s57, s56, -11
	s_bitcmp0_b32 s57, 6
	s_cselect_b64 vcc, -1, 0
	v_cndmask_b32_e32 v2, v79, v78, vcc
	s_nop 0
	v_readlane_b32 s57, v2, s57
	s_lshl_b32 s57, s57, 10
	s_add_i32 s57, s57, 0x1000000
	s_nop 2
	buffer_load_dwordx4 v[2:5], v0, s[92:95], s57 offen
	s_add_i32 s57, s56, -10
	s_bitcmp0_b32 s57, 6
	s_cselect_b64 vcc, -1, 0
	v_cndmask_b32_e32 v22, v79, v78, vcc
	s_nop 0
	v_readlane_b32 s57, v22, s57
	s_lshl_b32 s57, s57, 10
	s_add_i32 s57, s57, 0x1000000
	s_nop 2
	buffer_load_dwordx4 v[22:25], v0, s[92:95], s57 offen
	s_add_i32 s57, s56, -9
	s_bitcmp0_b32 s57, 6
	s_cselect_b64 vcc, -1, 0
	v_cndmask_b32_e32 v38, v79, v78, vcc
	s_nop 0
	v_readlane_b32 s57, v38, s57
	s_lshl_b32 s57, s57, 10
	s_add_i32 s57, s57, 0x1000000
	s_nop 2
	buffer_load_dwordx4 v[38:41], v0, s[92:95], s57 offen
	s_add_i32 s57, s56, -8
	s_bitcmp0_b32 s57, 6
	s_cselect_b64 vcc, -1, 0
	v_cndmask_b32_e32 v54, v79, v78, vcc
	s_nop 0
	v_readlane_b32 s57, v54, s57
	s_lshl_b32 s57, s57, 10
	s_add_i32 s57, s57, 0x1000000
	s_nop 2
	buffer_load_dwordx4 v[54:57], v0, s[92:95], s57 offen
	s_add_i32 s57, s56, 0xffffff69
	s_waitcnt vmcnt(5)
	v_perm_b32 v112, v26, v10, s67
	v_perm_b32 v10, v26, v10, s68
	s_waitcnt vmcnt(3)
	v_perm_b32 v26, v58, v42, s67
	v_readlane_b32 s57, v111, s57
	v_perm_b32 v42, v58, v42, s68
	v_perm_b32 v58, v26, v112, s69
	v_perm_b32 v26, v26, v112, s33
	v_perm_b32 v112, v42, v10, s69
	v_perm_b32 v10, v42, v10, s33
	v_dot4c_i32_i8_e32 v74, s57, v26
	v_and_b32_e32 v26, 0xf0f0f0f0, v26
	v_dot4c_i32_i8_e32 v70, s57, v26
	v_and_b32_e32 v26, 0xf0f0f0f0, v112
	v_dot4c_i32_i8_e32 v76, s57, v10
	v_and_b32_e32 v10, 0xf0f0f0f0, v10
	v_and_b32_e32 v42, 0xf0f0f0f0, v58
	v_dot4c_i32_i8_e32 v72, s57, v26
	v_dot4c_i32_i8_e32 v73, s57, v10
	v_perm_b32 v10, v27, v11, s67
	v_perm_b32 v26, v59, v43, s67
	v_dot4c_i32_i8_e32 v69, s57, v42
	v_perm_b32 v11, v27, v11, s68
	v_perm_b32 v27, v59, v43, s68
	v_perm_b32 v42, v26, v10, s69
	v_perm_b32 v10, v26, v10, s33
	v_perm_b32 v26, v27, v11, s69
	v_dot4c_i32_i8_e32 v85, s57, v10
	v_and_b32_e32 v10, 0xf0f0f0f0, v10
	v_perm_b32 v11, v27, v11, s33
	v_dot4c_i32_i8_e32 v81, s57, v10
	v_and_b32_e32 v10, 0xf0f0f0f0, v26
	v_dot4c_i32_i8_e32 v82, s57, v10
	v_and_b32_e32 v10, 0xf0f0f0f0, v11
	v_and_b32_e32 v27, 0xf0f0f0f0, v42
	v_dot4c_i32_i8_e32 v94, s57, v11
	v_dot4c_i32_i8_e32 v84, s57, v10
	v_perm_b32 v10, v28, v12, s67
	v_perm_b32 v11, v28, v12, s68
	v_perm_b32 v12, v60, v44, s67
	v_dot4c_i32_i8_e32 v77, s57, v27
	v_dot4c_i32_i8_e32 v86, s57, v26
	v_perm_b32 v26, v60, v44, s68
	v_perm_b32 v27, v12, v10, s69
	v_perm_b32 v10, v12, v10, s33
	v_perm_b32 v12, v26, v11, s69
	v_dot4c_i32_i8_e32 v96, s57, v10
	v_and_b32_e32 v10, 0xf0f0f0f0, v10
	v_perm_b32 v11, v26, v11, s33
	v_dot4c_i32_i8_e32 v88, s57, v10
	v_and_b32_e32 v10, 0xf0f0f0f0, v12
	v_dot4c_i32_i8_e32 v89, s57, v10
	v_and_b32_e32 v10, 0xf0f0f0f0, v11
	v_and_b32_e32 v26, 0xf0f0f0f0, v27
	v_dot4c_i32_i8_e32 v97, s57, v12
	v_dot4c_i32_i8_e32 v90, s57, v10
	v_perm_b32 v10, v29, v13, s67
	v_perm_b32 v12, v61, v45, s67
	v_dot4c_i32_i8_e32 v87, s57, v26
	v_dot4c_i32_i8_e32 v98, s57, v11
	v_perm_b32 v11, v29, v13, s68
	v_perm_b32 v13, v61, v45, s68
	v_perm_b32 v26, v12, v10, s69
	v_perm_b32 v10, v12, v10, s33
	v_perm_b32 v12, v13, v11, s69
	v_dot4c_i32_i8_e32 v100, s57, v10
	v_and_b32_e32 v10, 0xf0f0f0f0, v10
	v_perm_b32 v11, v13, v11, s33
	v_dot4c_i32_i8_e32 v92, s57, v10
	v_and_b32_e32 v10, 0xf0f0f0f0, v12
	v_and_b32_e32 v13, 0xf0f0f0f0, v26
	v_dot4c_i32_i8_e32 v93, s57, v10
	v_and_b32_e32 v10, 0xf0f0f0f0, v11
	v_dot4c_i32_i8_e32 v66, s57, v58
	v_dot4c_i32_i8_e32 v75, s57, v112
	v_dot4c_i32_i8_e32 v80, s57, v42
	v_dot4c_i32_i8_e32 v95, s57, v27
	v_dot4c_i32_i8_e32 v99, s57, v26
	v_dot4c_i32_i8_e32 v91, s57, v13
	v_dot4c_i32_i8_e32 v101, s57, v12
	v_dot4c_i32_i8_e32 v102, s57, v11
	v_dot4c_i32_i8_e32 v83, s57, v10
	s_add_i32 s57, s56, -7
	s_bitcmp0_b32 s57, 6
	s_cselect_b64 vcc, -1, 0
	v_cndmask_b32_e32 v10, v79, v78, vcc
	s_nop 0
	v_readlane_b32 s57, v10, s57
	s_lshl_b32 s57, s57, 10
	s_add_i32 s57, s57, 0x1000000
	s_nop 2
	buffer_load_dwordx4 v[10:13], v0, s[92:95], s57 offen
	s_add_i32 s57, s56, -6
	s_bitcmp0_b32 s57, 6
	s_cselect_b64 vcc, -1, 0
	v_cndmask_b32_e32 v26, v79, v78, vcc
	s_nop 0
	v_readlane_b32 s57, v26, s57
	s_lshl_b32 s57, s57, 10
	s_add_i32 s57, s57, 0x1000000
	s_nop 2
	buffer_load_dwordx4 v[26:29], v0, s[92:95], s57 offen
	s_add_i32 s57, s56, -5
	s_bitcmp0_b32 s57, 6
	s_cselect_b64 vcc, -1, 0
	v_cndmask_b32_e32 v42, v79, v78, vcc
	s_nop 0
	v_readlane_b32 s57, v42, s57
	s_lshl_b32 s57, s57, 10
	s_add_i32 s57, s57, 0x1000000
	s_nop 2
	buffer_load_dwordx4 v[42:45], v0, s[92:95], s57 offen
	s_add_i32 s57, s56, -4
	s_bitcmp0_b32 s57, 6
	s_cselect_b64 vcc, -1, 0
	v_cndmask_b32_e32 v58, v79, v78, vcc
	s_nop 0
	v_readlane_b32 s57, v58, s57
	s_lshl_b32 s57, s57, 10
	s_add_i32 s57, s57, 0x1000000
	s_nop 2
	buffer_load_dwordx4 v[58:61], v0, s[92:95], s57 offen
	s_add_i32 s57, s56, 0xffffff6d
	s_waitcnt vmcnt(5)
; __device__ __forceinline__ int shl_i(int v, int from_lane) { return __builtin_amdgcn_ds_bpermute(from_lane << 2, v); }
;     ...
;         const int pk0 = (q0 & 0xFF) | ((shl_i(q0, lane + 1) & 0xFF) << 8) | ((shl_i(q0, lane + 2) & 0xFF) << 16) | (shl_i(q0, lane + 3) << 24);
;         const int pk1 = (q1 & 0xFF) | ((shl_i(q1, lane + 1) & 0xFF) << 8) | ((shl_i(q1, lane + 2) & 0xFF) << 16) | (shl_i(q1, lane + 3) << 24);
	v_perm_b32 v112, v34, v18, s67
	v_perm_b32 v18, v34, v18, s68
	s_waitcnt vmcnt(3)
	v_perm_b32 v34, v62, v50, s67
	v_readlane_b32 s57, v111, s57
	v_perm_b32 v50, v62, v50, s68
	v_perm_b32 v62, v34, v112, s69
	v_perm_b32 v34, v34, v112, s33
	v_perm_b32 v112, v50, v18, s69
	v_perm_b32 v18, v50, v18, s33
	v_dot4c_i32_i8_e32 v74, s57, v34
	v_and_b32_e32 v34, 0xf0f0f0f0, v34
	v_dot4c_i32_i8_e32 v70, s57, v34
	v_and_b32_e32 v34, 0xf0f0f0f0, v112
	v_dot4c_i32_i8_e32 v76, s57, v18
	v_and_b32_e32 v18, 0xf0f0f0f0, v18
	v_and_b32_e32 v50, 0xf0f0f0f0, v62
	v_dot4c_i32_i8_e32 v72, s57, v34
	v_dot4c_i32_i8_e32 v73, s57, v18
	v_perm_b32 v18, v35, v19, s67
	v_perm_b32 v34, v63, v51, s67
	v_dot4c_i32_i8_e32 v69, s57, v50
	v_perm_b32 v19, v35, v19, s68
	v_perm_b32 v35, v63, v51, s68
	v_perm_b32 v50, v34, v18, s69
	v_perm_b32 v18, v34, v18, s33
	v_perm_b32 v34, v35, v19, s69
	v_dot4c_i32_i8_e32 v85, s57, v18
	v_and_b32_e32 v18, 0xf0f0f0f0, v18
	v_perm_b32 v19, v35, v19, s33
	v_dot4c_i32_i8_e32 v81, s57, v18
	v_and_b32_e32 v18, 0xf0f0f0f0, v34
	v_dot4c_i32_i8_e32 v82, s57, v18
	v_and_b32_e32 v18, 0xf0f0f0f0, v19
	v_and_b32_e32 v35, 0xf0f0f0f0, v50
	v_dot4c_i32_i8_e32 v94, s57, v19
	v_dot4c_i32_i8_e32 v84, s57, v18
	v_perm_b32 v18, v36, v20, s67
	v_perm_b32 v19, v36, v20, s68
	v_perm_b32 v20, v64, v52, s67
	v_dot4c_i32_i8_e32 v77, s57, v35
	v_dot4c_i32_i8_e32 v86, s57, v34
	v_perm_b32 v34, v64, v52, s68
	v_perm_b32 v35, v20, v18, s69
	v_perm_b32 v18, v20, v18, s33
	v_perm_b32 v20, v34, v19, s69
	v_dot4c_i32_i8_e32 v96, s57, v18
	v_and_b32_e32 v18, 0xf0f0f0f0, v18
	v_perm_b32 v19, v34, v19, s33
	v_dot4c_i32_i8_e32 v88, s57, v18
	v_and_b32_e32 v18, 0xf0f0f0f0, v20
	v_dot4c_i32_i8_e32 v89, s57, v18
	v_and_b32_e32 v18, 0xf0f0f0f0, v19
	v_and_b32_e32 v34, 0xf0f0f0f0, v35
	v_dot4c_i32_i8_e32 v97, s57, v20
	v_dot4c_i32_i8_e32 v90, s57, v18
	v_perm_b32 v18, v37, v21, s67
	v_perm_b32 v20, v65, v53, s67
	v_dot4c_i32_i8_e32 v87, s57, v34
	v_dot4c_i32_i8_e32 v98, s57, v19
	v_perm_b32 v19, v37, v21, s68
	v_perm_b32 v21, v65, v53, s68
	v_perm_b32 v34, v20, v18, s69
	v_perm_b32 v18, v20, v18, s33
	v_perm_b32 v20, v21, v19, s69
	v_dot4c_i32_i8_e32 v100, s57, v18
	v_and_b32_e32 v18, 0xf0f0f0f0, v18
	v_perm_b32 v19, v21, v19, s33
	v_dot4c_i32_i8_e32 v92, s57, v18
	v_and_b32_e32 v18, 0xf0f0f0f0, v20
	v_and_b32_e32 v21, 0xf0f0f0f0, v34
	v_dot4c_i32_i8_e32 v93, s57, v18
	v_and_b32_e32 v18, 0xf0f0f0f0, v19
	v_dot4c_i32_i8_e32 v66, s57, v62
	v_dot4c_i32_i8_e32 v75, s57, v112
	v_dot4c_i32_i8_e32 v80, s57, v50
	v_dot4c_i32_i8_e32 v95, s57, v35
	v_dot4c_i32_i8_e32 v99, s57, v34
	v_dot4c_i32_i8_e32 v91, s57, v21
	v_dot4c_i32_i8_e32 v101, s57, v20
	v_dot4c_i32_i8_e32 v102, s57, v19
	v_dot4c_i32_i8_e32 v83, s57, v18
	s_add_i32 s57, s56, -3
	s_bitcmp0_b32 s57, 6
	s_cselect_b64 vcc, -1, 0
	v_cndmask_b32_e32 v18, v79, v78, vcc
	s_nop 0
	v_readlane_b32 s57, v18, s57
	s_lshl_b32 s57, s57, 10
	s_add_i32 s57, s57, 0x1000000
	s_nop 2
	buffer_load_dwordx4 v[18:21], v0, s[92:95], s57 offen
	s_add_i32 s57, s56, -2
	s_bitcmp0_b32 s57, 6
	s_cselect_b64 vcc, -1, 0
	v_cndmask_b32_e32 v34, v79, v78, vcc
	s_nop 0
	v_readlane_b32 s57, v34, s57
	s_lshl_b32 s57, s57, 10
	s_add_i32 s57, s57, 0x1000000
	s_nop 2
	buffer_load_dwordx4 v[34:37], v0, s[92:95], s57 offen
	s_add_i32 s57, s56, -1
	s_bitcmp0_b32 s57, 6
	s_cselect_b64 vcc, -1, 0
	v_cndmask_b32_e32 v50, v79, v78, vcc
	s_nop 0
	v_readlane_b32 s57, v50, s57
	s_lshl_b32 s57, s57, 10
	s_add_i32 s57, s57, 0x1000000
	s_bitcmp0_b32 s56, 6
	s_cselect_b64 vcc, -1, 0
	v_cndmask_b32_e32 v62, v79, v78, vcc
	buffer_load_dwordx4 v[50:53], v0, s[92:95], s57 offen
	v_readlane_b32 s57, v62, s56
	s_lshl_b32 s57, s57, 10
	s_add_i32 s57, s57, 0x1000000
	s_nop 2
	buffer_load_dwordx4 v[62:65], v0, s[92:95], s57 offen
	s_add_i32 s56, s56, 16
	s_cmpk_lg_i32 s56, 0xdf
	s_cbranch_scc1 .LBB0_1423
	v_min_u32_e32 v111, v105, v106
	v_max_u32_e32 v105, v105, v106
	v_cndmask_b32_e64 v200, v105, v111, s[6:7]
	v_lshlrev_b32_e32 v105, 8, v108
	v_lshlrev_b32_e32 v106, 16, v109
	s_mov_b32 s56, 0xc0c0500
	v_lshlrev_b32_e32 v108, 24, v110
	v_perm_b32 v105, v105, v107, s56
	v_and_b32_e32 v106, 0xff0000, v106
	v_lshrrev_b32_e32 v199, 16, v200
	v_or3_b32 v105, v105, v106, v108
	s_mov_b32 s62, 0
	s_movk_i32 s63, 0xdf
	s_mov_b32 s90, 0x1be0000
	s_cmp_eq_u32 s101, 0
	s_cbranch_scc1 .Lnb_1425
	s_barrier
.Lnb_1425:
.LBB0_1425:
	s_add_i32 s56, s63, 0xffffff21
	s_waitcnt vmcnt(5)
	v_perm_b32 v106, v14, v6, s67
	v_perm_b32 v6, v14, v6, s68
	s_waitcnt vmcnt(3)
	v_perm_b32 v14, v46, v30, s67
	v_readlane_b32 s56, v105, s56
	v_perm_b32 v30, v46, v30, s68
	v_perm_b32 v46, v14, v106, s69
	v_perm_b32 v14, v14, v106, s33
	v_perm_b32 v106, v30, v6, s69
	v_perm_b32 v6, v30, v6, s33
	v_dot4c_i32_i8_e32 v74, s56, v14
	v_and_b32_e32 v14, 0xf0f0f0f0, v14
	v_dot4c_i32_i8_e32 v70, s56, v14
	v_and_b32_e32 v14, 0xf0f0f0f0, v106
	v_dot4c_i32_i8_e32 v76, s56, v6
	v_and_b32_e32 v6, 0xf0f0f0f0, v6
	v_and_b32_e32 v30, 0xf0f0f0f0, v46
	v_dot4c_i32_i8_e32 v72, s56, v14
	v_dot4c_i32_i8_e32 v73, s56, v6
	v_perm_b32 v6, v15, v7, s67
	v_perm_b32 v14, v47, v31, s67
	v_dot4c_i32_i8_e32 v69, s56, v30
	v_perm_b32 v7, v15, v7, s68
	v_perm_b32 v15, v47, v31, s68
	v_perm_b32 v30, v14, v6, s69
	v_perm_b32 v6, v14, v6, s33
	v_perm_b32 v14, v15, v7, s69
	v_dot4c_i32_i8_e32 v85, s56, v6
	v_and_b32_e32 v6, 0xf0f0f0f0, v6
	v_perm_b32 v7, v15, v7, s33
	v_dot4c_i32_i8_e32 v81, s56, v6
	v_and_b32_e32 v6, 0xf0f0f0f0, v14
	v_dot4c_i32_i8_e32 v82, s56, v6
	v_and_b32_e32 v6, 0xf0f0f0f0, v7
	v_and_b32_e32 v15, 0xf0f0f0f0, v30
	v_dot4c_i32_i8_e32 v94, s56, v7
	v_dot4c_i32_i8_e32 v84, s56, v6
	v_perm_b32 v6, v16, v8, s67
	v_perm_b32 v7, v16, v8, s68
	v_perm_b32 v8, v48, v32, s67
	v_dot4c_i32_i8_e32 v77, s56, v15
	v_dot4c_i32_i8_e32 v86, s56, v14
	v_perm_b32 v14, v48, v32, s68
	v_perm_b32 v15, v8, v6, s69
	v_perm_b32 v6, v8, v6, s33
	v_perm_b32 v8, v14, v7, s69
	v_dot4c_i32_i8_e32 v96, s56, v6
	v_and_b32_e32 v6, 0xf0f0f0f0, v6
	v_perm_b32 v7, v14, v7, s33
	v_dot4c_i32_i8_e32 v88, s56, v6
	v_and_b32_e32 v6, 0xf0f0f0f0, v8
	v_dot4c_i32_i8_e32 v89, s56, v6
	v_and_b32_e32 v6, 0xf0f0f0f0, v7
	v_and_b32_e32 v14, 0xf0f0f0f0, v15
	v_dot4c_i32_i8_e32 v97, s56, v8
	v_dot4c_i32_i8_e32 v90, s56, v6
	v_perm_b32 v6, v17, v9, s67
	v_perm_b32 v8, v49, v33, s67
	v_dot4c_i32_i8_e32 v87, s56, v14
	v_dot4c_i32_i8_e32 v98, s56, v7
	v_perm_b32 v7, v17, v9, s68
	v_perm_b32 v9, v49, v33, s68
	v_perm_b32 v14, v8, v6, s69
	v_perm_b32 v6, v8, v6, s33
	v_perm_b32 v8, v9, v7, s69
	v_dot4c_i32_i8_e32 v100, s56, v6
	v_and_b32_e32 v6, 0xf0f0f0f0, v6
	s_add_i32 s91, s63, -15
	v_perm_b32 v7, v9, v7, s33
	v_dot4c_i32_i8_e32 v92, s56, v6
	v_and_b32_e32 v6, 0xf0f0f0f0, v8
	s_cmp_gt_u32 s62, 2
	v_and_b32_e32 v9, 0xf0f0f0f0, v14
	v_dot4c_i32_i8_e32 v93, s56, v6
	v_and_b32_e32 v6, 0xf0f0f0f0, v7
	s_cselect_b64 vcc, -1, 0
	s_bitcmp0_b32 s91, 6
	v_dot4c_i32_i8_e32 v66, s56, v46
	v_dot4c_i32_i8_e32 v75, s56, v106
	v_dot4c_i32_i8_e32 v80, s56, v30
	v_dot4c_i32_i8_e32 v95, s56, v15
	v_dot4c_i32_i8_e32 v99, s56, v14
	v_dot4c_i32_i8_e32 v91, s56, v9
	v_dot4c_i32_i8_e32 v101, s56, v8
	v_dot4c_i32_i8_e32 v102, s56, v7
	v_dot4c_i32_i8_e32 v83, s56, v6
	s_cselect_b64 s[56:57], -1, 0
	v_cndmask_b32_e64 v6, v79, v78, s[56:57]
	v_cndmask_b32_e32 v6, v6, v199, vcc
	s_add_i32 s57, s90, 0xffe20000
	v_readlane_b32 s56, v6, s91
	s_lshl_b32 s56, s56, 10
	s_and_b32 s57, s57, 0x1000000
	s_add_i32 s56, s56, s57
	s_add_i32 s91, s63, -14
	s_bitcmp0_b32 s91, 6
	buffer_load_dwordx4 v[6:9], v0, s[92:95], s56 offen
	s_cselect_b64 s[56:57], -1, 0
	v_cndmask_b32_e64 v14, v79, v78, s[56:57]
	v_cndmask_b32_e32 v14, v14, v199, vcc
	s_add_i32 s57, s90, 0xffe40000
	v_readlane_b32 s56, v14, s91
	s_lshl_b32 s56, s56, 10
	s_and_b32 s57, s57, 0x1000000
	s_add_i32 s56, s56, s57
	s_add_i32 s91, s63, -13
	s_bitcmp0_b32 s91, 6
	buffer_load_dwordx4 v[14:17], v0, s[92:95], s56 offen
	s_cselect_b64 s[56:57], -1, 0
	v_cndmask_b32_e64 v30, v79, v78, s[56:57]
	v_cndmask_b32_e32 v30, v30, v199, vcc
	s_add_i32 s57, s90, 0xffe60000
	v_readlane_b32 s56, v30, s91
	s_lshl_b32 s56, s56, 10
	s_and_b32 s57, s57, 0x1000000
	s_add_i32 s56, s56, s57
	s_add_i32 s91, s63, -12
	s_bitcmp0_b32 s91, 6
	buffer_load_dwordx4 v[30:33], v0, s[92:95], s56 offen
	s_cselect_b64 s[56:57], -1, 0
	v_cndmask_b32_e64 v46, v79, v78, s[56:57]
	v_cndmask_b32_e32 v46, v46, v199, vcc
	s_add_i32 s57, s90, 0xffe80000
	v_readlane_b32 s56, v46, s91
	s_lshl_b32 s56, s56, 10
	s_and_b32 s57, s57, 0x1000000
	s_add_i32 s56, s56, s57
	s_nop 1
	buffer_load_dwordx4 v[46:49], v0, s[92:95], s56 offen
	s_add_i32 s56, s63, 0xffffff25
	s_waitcnt vmcnt(5)
	v_perm_b32 v106, v22, v2, s67
	v_perm_b32 v2, v22, v2, s68
	s_waitcnt vmcnt(3)
	v_perm_b32 v22, v54, v38, s67
	v_readlane_b32 s56, v105, s56
	v_perm_b32 v38, v54, v38, s68
	v_perm_b32 v54, v22, v106, s69
	v_perm_b32 v22, v22, v106, s33
	v_perm_b32 v106, v38, v2, s69
	v_perm_b32 v2, v38, v2, s33
	v_dot4c_i32_i8_e32 v74, s56, v22
	v_and_b32_e32 v22, 0xf0f0f0f0, v22
	v_dot4c_i32_i8_e32 v70, s56, v22
	v_and_b32_e32 v22, 0xf0f0f0f0, v106
	v_dot4c_i32_i8_e32 v76, s56, v2
	v_and_b32_e32 v2, 0xf0f0f0f0, v2
	v_and_b32_e32 v38, 0xf0f0f0f0, v54
	v_dot4c_i32_i8_e32 v72, s56, v22
	v_dot4c_i32_i8_e32 v73, s56, v2
	v_perm_b32 v2, v23, v3, s67
	v_perm_b32 v22, v55, v39, s67
	v_dot4c_i32_i8_e32 v69, s56, v38
	v_perm_b32 v3, v23, v3, s68
	v_perm_b32 v23, v55, v39, s68
	v_perm_b32 v38, v22, v2, s69
	v_perm_b32 v2, v22, v2, s33
	v_perm_b32 v22, v23, v3, s69
	v_dot4c_i32_i8_e32 v85, s56, v2
	v_and_b32_e32 v2, 0xf0f0f0f0, v2
	v_perm_b32 v3, v23, v3, s33
	v_dot4c_i32_i8_e32 v81, s56, v2
	v_and_b32_e32 v2, 0xf0f0f0f0, v22
	v_dot4c_i32_i8_e32 v82, s56, v2
	v_and_b32_e32 v2, 0xf0f0f0f0, v3
	v_and_b32_e32 v23, 0xf0f0f0f0, v38
	v_dot4c_i32_i8_e32 v94, s56, v3
	v_dot4c_i32_i8_e32 v84, s56, v2
	v_perm_b32 v2, v24, v4, s67
	v_perm_b32 v3, v24, v4, s68
	v_perm_b32 v4, v56, v40, s67
	v_dot4c_i32_i8_e32 v77, s56, v23
	v_dot4c_i32_i8_e32 v86, s56, v22
	v_perm_b32 v22, v56, v40, s68
	v_perm_b32 v23, v4, v2, s69
	v_perm_b32 v2, v4, v2, s33
	v_perm_b32 v4, v22, v3, s69
	v_dot4c_i32_i8_e32 v96, s56, v2
	v_and_b32_e32 v2, 0xf0f0f0f0, v2
	v_perm_b32 v3, v22, v3, s33
	v_dot4c_i32_i8_e32 v88, s56, v2
	v_and_b32_e32 v2, 0xf0f0f0f0, v4
	v_dot4c_i32_i8_e32 v89, s56, v2
	v_and_b32_e32 v2, 0xf0f0f0f0, v3
	v_and_b32_e32 v22, 0xf0f0f0f0, v23
	v_dot4c_i32_i8_e32 v97, s56, v4
	v_dot4c_i32_i8_e32 v90, s56, v2
	v_perm_b32 v2, v25, v5, s67
	v_perm_b32 v4, v57, v41, s67
	v_dot4c_i32_i8_e32 v87, s56, v22
	v_dot4c_i32_i8_e32 v98, s56, v3
	v_perm_b32 v3, v25, v5, s68
	v_perm_b32 v5, v57, v41, s68
	v_perm_b32 v22, v4, v2, s69
	v_perm_b32 v2, v4, v2, s33
	v_perm_b32 v4, v5, v3, s69
	v_dot4c_i32_i8_e32 v100, s56, v2
	v_and_b32_e32 v2, 0xf0f0f0f0, v2
	v_perm_b32 v3, v5, v3, s33
	v_dot4c_i32_i8_e32 v92, s56, v2
	v_and_b32_e32 v2, 0xf0f0f0f0, v4
	s_add_i32 s91, s63, -11
	v_and_b32_e32 v5, 0xf0f0f0f0, v22
	v_dot4c_i32_i8_e32 v93, s56, v2
	v_and_b32_e32 v2, 0xf0f0f0f0, v3
	s_bitcmp0_b32 s91, 6
	v_dot4c_i32_i8_e32 v66, s56, v54
	v_dot4c_i32_i8_e32 v75, s56, v106
	v_dot4c_i32_i8_e32 v80, s56, v38
	v_dot4c_i32_i8_e32 v95, s56, v23
	v_dot4c_i32_i8_e32 v99, s56, v22
	v_dot4c_i32_i8_e32 v91, s56, v5
	v_dot4c_i32_i8_e32 v101, s56, v4
	v_dot4c_i32_i8_e32 v102, s56, v3
	v_dot4c_i32_i8_e32 v83, s56, v2
	s_cselect_b64 s[56:57], -1, 0
	v_cndmask_b32_e64 v2, v79, v78, s[56:57]
	v_cndmask_b32_e32 v2, v2, v199, vcc
	s_add_i32 s57, s90, 0xffea0000
	v_readlane_b32 s56, v2, s91
	s_lshl_b32 s56, s56, 10
	s_and_b32 s57, s57, 0x1000000
	s_add_i32 s56, s56, s57
	s_add_i32 s91, s63, -10
	s_bitcmp0_b32 s91, 6
	buffer_load_dwordx4 v[2:5], v0, s[92:95], s56 offen
	s_cselect_b64 s[56:57], -1, 0
	v_cndmask_b32_e64 v22, v79, v78, s[56:57]
	v_cndmask_b32_e32 v22, v22, v199, vcc
	s_add_i32 s57, s90, 0xffec0000
	v_readlane_b32 s56, v22, s91
	s_lshl_b32 s56, s56, 10
	s_and_b32 s57, s57, 0x1000000
	s_add_i32 s56, s56, s57
	s_add_i32 s91, s63, -9
	s_bitcmp0_b32 s91, 6
	buffer_load_dwordx4 v[22:25], v0, s[92:95], s56 offen
	s_cselect_b64 s[56:57], -1, 0
	v_cndmask_b32_e64 v38, v79, v78, s[56:57]
	v_cndmask_b32_e32 v38, v38, v199, vcc
	s_add_i32 s57, s90, 0xffee0000
	v_readlane_b32 s56, v38, s91
	s_lshl_b32 s56, s56, 10
	s_and_b32 s57, s57, 0x1000000
	s_add_i32 s56, s56, s57
	s_add_i32 s91, s63, -8
	s_bitcmp0_b32 s91, 6
	buffer_load_dwordx4 v[38:41], v0, s[92:95], s56 offen
	s_cselect_b64 s[56:57], -1, 0
	v_cndmask_b32_e64 v54, v79, v78, s[56:57]
	v_cndmask_b32_e32 v54, v54, v199, vcc
	s_add_i32 s57, s90, 0xfff00000
	v_readlane_b32 s56, v54, s91
	s_lshl_b32 s56, s56, 10
	s_and_b32 s57, s57, 0x1000000
	s_add_i32 s56, s56, s57
	s_nop 1
	buffer_load_dwordx4 v[54:57], v0, s[92:95], s56 offen
	s_add_i32 s56, s63, 0xffffff29
	s_waitcnt vmcnt(5)
	v_perm_b32 v106, v26, v10, s67
	v_perm_b32 v10, v26, v10, s68
	s_waitcnt vmcnt(3)
	v_perm_b32 v26, v58, v42, s67
	v_readlane_b32 s56, v105, s56
	v_perm_b32 v42, v58, v42, s68
	v_perm_b32 v58, v26, v106, s69
	v_perm_b32 v26, v26, v106, s33
	v_perm_b32 v106, v42, v10, s69
	v_perm_b32 v10, v42, v10, s33
	v_dot4c_i32_i8_e32 v74, s56, v26
	v_and_b32_e32 v26, 0xf0f0f0f0, v26
	v_dot4c_i32_i8_e32 v70, s56, v26
	v_and_b32_e32 v26, 0xf0f0f0f0, v106
	v_dot4c_i32_i8_e32 v76, s56, v10
	v_and_b32_e32 v10, 0xf0f0f0f0, v10
	v_and_b32_e32 v42, 0xf0f0f0f0, v58
	v_dot4c_i32_i8_e32 v72, s56, v26
	v_dot4c_i32_i8_e32 v73, s56, v10
	v_perm_b32 v10, v27, v11, s67
	v_perm_b32 v26, v59, v43, s67
	v_dot4c_i32_i8_e32 v69, s56, v42
	v_perm_b32 v11, v27, v11, s68
	v_perm_b32 v27, v59, v43, s68
	v_perm_b32 v42, v26, v10, s69
	v_perm_b32 v10, v26, v10, s33
	v_perm_b32 v26, v27, v11, s69
	v_dot4c_i32_i8_e32 v85, s56, v10
	v_and_b32_e32 v10, 0xf0f0f0f0, v10
	v_perm_b32 v11, v27, v11, s33
	v_dot4c_i32_i8_e32 v81, s56, v10
	v_and_b32_e32 v10, 0xf0f0f0f0, v26
	v_dot4c_i32_i8_e32 v82, s56, v10
	v_and_b32_e32 v10, 0xf0f0f0f0, v11
	v_and_b32_e32 v27, 0xf0f0f0f0, v42
	v_dot4c_i32_i8_e32 v94, s56, v11
	v_dot4c_i32_i8_e32 v84, s56, v10
	v_perm_b32 v10, v28, v12, s67
	v_perm_b32 v11, v28, v12, s68
	v_perm_b32 v12, v60, v44, s67
	v_dot4c_i32_i8_e32 v77, s56, v27
	v_dot4c_i32_i8_e32 v86, s56, v26
	v_perm_b32 v26, v60, v44, s68
	v_perm_b32 v27, v12, v10, s69
	v_perm_b32 v10, v12, v10, s33
	v_perm_b32 v12, v26, v11, s69
	v_dot4c_i32_i8_e32 v96, s56, v10
	v_and_b32_e32 v10, 0xf0f0f0f0, v10
	v_perm_b32 v11, v26, v11, s33
	v_dot4c_i32_i8_e32 v88, s56, v10
	v_and_b32_e32 v10, 0xf0f0f0f0, v12
	v_dot4c_i32_i8_e32 v89, s56, v10
	v_and_b32_e32 v10, 0xf0f0f0f0, v11
	v_and_b32_e32 v26, 0xf0f0f0f0, v27
	v_dot4c_i32_i8_e32 v97, s56, v12
	v_dot4c_i32_i8_e32 v90, s56, v10
	v_perm_b32 v10, v29, v13, s67
	v_perm_b32 v12, v61, v45, s67
	v_dot4c_i32_i8_e32 v87, s56, v26
	v_dot4c_i32_i8_e32 v98, s56, v11
	v_perm_b32 v11, v29, v13, s68
	v_perm_b32 v13, v61, v45, s68
	v_perm_b32 v26, v12, v10, s69
	v_perm_b32 v10, v12, v10, s33
	v_perm_b32 v12, v13, v11, s69
	v_dot4c_i32_i8_e32 v100, s56, v10
	v_and_b32_e32 v10, 0xf0f0f0f0, v10
	v_perm_b32 v11, v13, v11, s33
	v_dot4c_i32_i8_e32 v92, s56, v10
	v_and_b32_e32 v10, 0xf0f0f0f0, v12
	s_add_i32 s91, s63, -7
	v_and_b32_e32 v13, 0xf0f0f0f0, v26
	v_dot4c_i32_i8_e32 v93, s56, v10
	v_and_b32_e32 v10, 0xf0f0f0f0, v11
	s_bitcmp0_b32 s91, 6
	v_dot4c_i32_i8_e32 v66, s56, v58
	v_dot4c_i32_i8_e32 v75, s56, v106
	v_dot4c_i32_i8_e32 v80, s56, v42
	v_dot4c_i32_i8_e32 v95, s56, v27
	v_dot4c_i32_i8_e32 v99, s56, v26
	v_dot4c_i32_i8_e32 v91, s56, v13
	v_dot4c_i32_i8_e32 v101, s56, v12
	v_dot4c_i32_i8_e32 v102, s56, v11
	v_dot4c_i32_i8_e32 v83, s56, v10
	s_cselect_b64 s[56:57], -1, 0
	v_cndmask_b32_e64 v10, v79, v78, s[56:57]
	v_cndmask_b32_e32 v10, v10, v199, vcc
	s_add_i32 s57, s90, 0xfff20000
	v_readlane_b32 s56, v10, s91
	s_lshl_b32 s56, s56, 10
	s_and_b32 s57, s57, 0x1000000
	s_add_i32 s56, s56, s57
	s_add_i32 s91, s63, -6
	s_bitcmp0_b32 s91, 6
	buffer_load_dwordx4 v[10:13], v0, s[92:95], s56 offen
	s_cselect_b64 s[56:57], -1, 0
	v_cndmask_b32_e64 v26, v79, v78, s[56:57]
	v_cndmask_b32_e32 v26, v26, v199, vcc
	s_add_i32 s57, s90, 0xfff40000
	v_readlane_b32 s56, v26, s91
	s_lshl_b32 s56, s56, 10
	s_and_b32 s57, s57, 0x1000000
	s_add_i32 s56, s56, s57
	s_add_i32 s91, s63, -5
	s_bitcmp0_b32 s91, 6
	buffer_load_dwordx4 v[26:29], v0, s[92:95], s56 offen
	s_cselect_b64 s[56:57], -1, 0
	v_cndmask_b32_e64 v42, v79, v78, s[56:57]
	v_cndmask_b32_e32 v42, v42, v199, vcc
	s_add_i32 s57, s90, 0xfff60000
	v_readlane_b32 s56, v42, s91
	s_lshl_b32 s56, s56, 10
	s_and_b32 s57, s57, 0x1000000
	s_add_i32 s56, s56, s57
	s_add_i32 s91, s63, -4
	s_bitcmp0_b32 s91, 6
	buffer_load_dwordx4 v[42:45], v0, s[92:95], s56 offen
	s_cselect_b64 s[56:57], -1, 0
	v_cndmask_b32_e64 v58, v79, v78, s[56:57]
	v_cndmask_b32_e32 v58, v58, v199, vcc
	s_add_i32 s57, s90, 0xfff80000
	v_readlane_b32 s56, v58, s91
	s_lshl_b32 s56, s56, 10
	s_and_b32 s57, s57, 0x1000000
	s_add_i32 s56, s56, s57
	s_nop 1
	buffer_load_dwordx4 v[58:61], v0, s[92:95], s56 offen
	s_add_i32 s56, s63, 0xffffff2d
	s_waitcnt vmcnt(5)
	v_perm_b32 v106, v34, v18, s67
	v_perm_b32 v18, v34, v18, s68
	s_waitcnt vmcnt(3)
	v_perm_b32 v34, v62, v50, s67
	v_readlane_b32 s56, v105, s56
	v_perm_b32 v50, v62, v50, s68
	v_perm_b32 v62, v34, v106, s69
	v_perm_b32 v34, v34, v106, s33
	v_perm_b32 v106, v50, v18, s69
	v_perm_b32 v18, v50, v18, s33
	v_dot4c_i32_i8_e32 v74, s56, v34
	v_and_b32_e32 v34, 0xf0f0f0f0, v34
	v_dot4c_i32_i8_e32 v70, s56, v34
	v_and_b32_e32 v34, 0xf0f0f0f0, v106
	v_dot4c_i32_i8_e32 v76, s56, v18
	v_and_b32_e32 v18, 0xf0f0f0f0, v18
	v_and_b32_e32 v50, 0xf0f0f0f0, v62
	v_dot4c_i32_i8_e32 v72, s56, v34
	v_dot4c_i32_i8_e32 v73, s56, v18
	v_perm_b32 v18, v35, v19, s67
	v_perm_b32 v34, v63, v51, s67
	v_dot4c_i32_i8_e32 v69, s56, v50
	v_perm_b32 v19, v35, v19, s68
	v_perm_b32 v35, v63, v51, s68
	v_perm_b32 v50, v34, v18, s69
	v_perm_b32 v18, v34, v18, s33
	v_perm_b32 v34, v35, v19, s69
	v_dot4c_i32_i8_e32 v85, s56, v18
	v_and_b32_e32 v18, 0xf0f0f0f0, v18
	v_perm_b32 v19, v35, v19, s33
	v_dot4c_i32_i8_e32 v81, s56, v18
	v_and_b32_e32 v18, 0xf0f0f0f0, v34
	v_dot4c_i32_i8_e32 v82, s56, v18
	v_and_b32_e32 v18, 0xf0f0f0f0, v19
	v_and_b32_e32 v35, 0xf0f0f0f0, v50
	v_dot4c_i32_i8_e32 v94, s56, v19
	v_dot4c_i32_i8_e32 v84, s56, v18
	v_perm_b32 v18, v36, v20, s67
	v_perm_b32 v19, v36, v20, s68
	v_perm_b32 v20, v64, v52, s67
	v_dot4c_i32_i8_e32 v77, s56, v35
	v_dot4c_i32_i8_e32 v86, s56, v34
	v_perm_b32 v34, v64, v52, s68
	v_perm_b32 v35, v20, v18, s69
	v_perm_b32 v18, v20, v18, s33
	v_perm_b32 v20, v34, v19, s69
	v_dot4c_i32_i8_e32 v96, s56, v18
	v_and_b32_e32 v18, 0xf0f0f0f0, v18
	v_perm_b32 v19, v34, v19, s33
	v_dot4c_i32_i8_e32 v88, s56, v18
	v_and_b32_e32 v18, 0xf0f0f0f0, v20
	v_dot4c_i32_i8_e32 v89, s56, v18
	v_and_b32_e32 v18, 0xf0f0f0f0, v19
	v_and_b32_e32 v34, 0xf0f0f0f0, v35
	v_dot4c_i32_i8_e32 v97, s56, v20
	v_dot4c_i32_i8_e32 v90, s56, v18
	v_perm_b32 v18, v37, v21, s67
	v_perm_b32 v20, v65, v53, s67
	v_dot4c_i32_i8_e32 v87, s56, v34
	v_dot4c_i32_i8_e32 v98, s56, v19
	v_perm_b32 v19, v37, v21, s68
	v_perm_b32 v21, v65, v53, s68
	v_perm_b32 v34, v20, v18, s69
	v_perm_b32 v18, v20, v18, s33
	v_perm_b32 v20, v21, v19, s69
	v_dot4c_i32_i8_e32 v100, s56, v18
	v_and_b32_e32 v18, 0xf0f0f0f0, v18
	v_perm_b32 v19, v21, v19, s33
	v_dot4c_i32_i8_e32 v92, s56, v18
	v_and_b32_e32 v18, 0xf0f0f0f0, v20
	s_add_i32 s91, s63, -3
	v_and_b32_e32 v21, 0xf0f0f0f0, v34
	v_dot4c_i32_i8_e32 v93, s56, v18
	v_and_b32_e32 v18, 0xf0f0f0f0, v19
	s_bitcmp0_b32 s91, 6
	v_dot4c_i32_i8_e32 v66, s56, v62
	v_dot4c_i32_i8_e32 v75, s56, v106
	v_dot4c_i32_i8_e32 v80, s56, v50
	v_dot4c_i32_i8_e32 v95, s56, v35
	v_dot4c_i32_i8_e32 v99, s56, v34
	v_dot4c_i32_i8_e32 v91, s56, v21
	v_dot4c_i32_i8_e32 v101, s56, v20
	v_dot4c_i32_i8_e32 v102, s56, v19
	v_dot4c_i32_i8_e32 v83, s56, v18
	s_cselect_b64 s[56:57], -1, 0
	v_cndmask_b32_e64 v18, v79, v78, s[56:57]
	v_cndmask_b32_e32 v18, v18, v199, vcc
	s_add_i32 s57, s90, 0xfffa0000
	v_readlane_b32 s56, v18, s91
	s_lshl_b32 s56, s56, 10
	s_and_b32 s57, s57, 0x1000000
	s_add_i32 s56, s56, s57
	s_add_i32 s91, s63, -2
	s_bitcmp0_b32 s91, 6
	buffer_load_dwordx4 v[18:21], v0, s[92:95], s56 offen
	s_cselect_b64 s[56:57], -1, 0
	v_cndmask_b32_e64 v34, v79, v78, s[56:57]
	v_cndmask_b32_e32 v34, v34, v199, vcc
	s_add_i32 s57, s90, 0xfffc0000
	v_readlane_b32 s56, v34, s91
	s_lshl_b32 s56, s56, 10
	s_and_b32 s57, s57, 0x1000000
	s_add_i32 s56, s56, s57
	s_add_i32 s91, s63, -1
	s_bitcmp0_b32 s91, 6
	buffer_load_dwordx4 v[34:37], v0, s[92:95], s56 offen
	s_cselect_b64 s[56:57], -1, 0
	v_cndmask_b32_e64 v50, v79, v78, s[56:57]
	v_cndmask_b32_e32 v50, v50, v199, vcc
	s_add_i32 s57, s90, 0xfffe0000
	v_readlane_b32 s56, v50, s91
	s_lshl_b32 s56, s56, 10
	s_and_b32 s57, s57, 0x1000000
	s_add_i32 s56, s56, s57
	s_bitcmp0_b32 s63, 6
	s_nop 0
	buffer_load_dwordx4 v[50:53], v0, s[92:95], s56 offen
	s_cselect_b64 s[56:57], -1, 0
	v_cndmask_b32_e64 v62, v79, v78, s[56:57]
	v_cndmask_b32_e32 v62, v62, v199, vcc
	s_and_b32 s57, s90, 0x1000000
	v_readlane_b32 s56, v62, s63
	s_lshl_b32 s56, s56, 10
	s_add_i32 s56, s56, s57
	s_nop 2
	buffer_load_dwordx4 v[62:65], v0, s[92:95], s56 offen
	s_add_i32 s62, s62, 1
	s_add_i32 s63, s63, 16
	s_add_i32 s90, s90, 0x200000
	s_cmpk_eq_i32 s63, 0x11f
	s_cbranch_scc0 .LBB0_1425
; __device__ __forceinline__ int ov(int x) { asm volatile("" : "+v"(x)); return x; }
;     ...
;         f32x2 acc[16];
;         { const float fsc = wm * (1.0f / 127.0f);
; #pragma unroll
;           for (int i = 0; i < 16; ++i) acc[i] = (f32x2){(float)(acci[2 * i] - acci[2 * i + 1] - c8) * fsc, (float)acci[2 * i + 1] * (fsc * 0.0625f)}; }
;         const int lane2 = ov(lane);
;         float s = 0.f;
; #pragma unroll
;         for (int hh = 0; hh < 4; ++hh) { float pl[8]; unpack8(*(const v4u*)(PLE + (size_t)t * D + lane2 * 32 + hh * 8), pl);
;             float z8[8]; unpack8(*(const v4u*)(ZB + (size_t)t * D + lane2 * 32 + hh * 8), z8);
;             f32x4 xa = (f32x4){z8[0], z8[1], z8[2], z8[3]}, xb = (f32x4){z8[4], z8[5], z8[6], z8[7]};
;             xa = (xa - mean1) * rstd1 * *(const f32x4*)(gain1 + lane2 * 32 + hh * 8) + *(const f32x4*)(bias1 + lane2 * 32 + hh * 8);
;             xb = (xb - mean1) * rstd1 * *(const f32x4*)(gain1 + lane2 * 32 + hh * 8 + 4) + *(const f32x4*)(bias1 + lane2 * 32 + hh * 8 + 4);
	s_waitcnt lgkmcnt(0)
	v_add_f32_e32 v78, v103, v104
	v_cvt_i32_f32_e32 v78, v78
	v_mov_b32_e32 v201, v130
	s_lshl_b64 s[56:57], s[86:87], 1
	v_lshlrev_b32_e32 v78, 3, v78
	v_sub_u32_e32 v78, 0, v78
	v_sub_u32_e32 v79, v78, v69
	v_add_u32_e32 v66, v79, v66
	v_sub_u32_e32 v79, v78, v70
	v_add_u32_e32 v74, v79, v74
	v_sub_u32_e32 v79, v78, v72
	v_add_u32_e32 v75, v79, v75
	v_sub_u32_e32 v79, v78, v73
	v_add_u32_e32 v76, v79, v76
	v_sub_u32_e32 v79, v78, v77
	v_add_u32_e32 v79, v79, v80
	v_sub_u32_e32 v80, v78, v81
	v_add_u32_e32 v80, v80, v85
	v_sub_u32_e32 v85, v78, v82
	v_add_u32_e32 v85, v85, v86
	v_sub_u32_e32 v86, v78, v84
	v_add_u32_e32 v86, v86, v94
	v_sub_u32_e32 v94, v78, v87
	v_add_u32_e32 v94, v94, v95
	v_sub_u32_e32 v95, v78, v88
	v_readlane_b32 s62, v255, 7
	v_lshlrev_b32_e32 v134, 5, v201
	v_add_u32_e32 v95, v95, v96
	v_sub_u32_e32 v96, v78, v89
	s_add_u32 s62, s62, s56
	v_readlane_b32 s63, v255, 9
	v_ashrrev_i32_e32 v135, 31, v134
	v_add_u32_e32 v96, v96, v97
	v_sub_u32_e32 v97, v78, v90
	v_cvt_f32_i32_e32 v181, v70
	v_mul_f32_e32 v142, 0x3c010204, v71
	s_addc_u32 s63, s63, s57
	v_lshlrev_b64 v[70:71], 1, v[134:135]
	v_add_u32_e32 v97, v97, v98
	v_sub_u32_e32 v98, v78, v91
	v_cvt_f32_i32_e32 v178, v75
	v_cvt_f32_i32_e32 v180, v74
	v_lshl_add_u64 v[74:75], s[62:63], 0, v[70:71]
	v_readlane_b32 s62, v254, 56
	v_add_u32_e32 v98, v98, v99
	v_sub_u32_e32 v99, v78, v92
	s_add_u32 s62, s62, s56
	v_readlane_b32 s63, v255, 5
	v_add_u32_e32 v99, v99, v100
	v_sub_u32_e32 v100, v78, v93
	v_sub_u32_e32 v78, v78, v83
	s_addc_u32 s63, s63, s57
	v_add_u32_e32 v100, v100, v101
	v_add_u32_e32 v78, v78, v102
	v_cvt_f32_i32_e32 v138, v99
	v_cvt_f32_i32_e32 v140, v98
	v_lshl_add_u64 v[98:99], s[62:63], 0, v[70:71]
	v_cvt_f32_i32_e32 v136, v100
	v_cvt_f32_i32_e32 v137, v93
	v_cvt_f32_i32_e32 v139, v92
	v_cvt_f32_i32_e32 v141, v91
	v_cvt_f32_i32_e32 v146, v97
	v_cvt_f32_i32_e32 v147, v90
	v_cvt_f32_i32_e32 v148, v96
	v_cvt_f32_i32_e32 v149, v89
	v_cvt_f32_i32_e32 v150, v95
	v_cvt_f32_i32_e32 v151, v88
	v_cvt_f32_i32_e32 v152, v94
	v_cvt_f32_i32_e32 v153, v87
	v_cvt_f32_i32_e32 v160, v86
	v_cvt_f32_i32_e32 v161, v84
	v_cvt_f32_i32_e32 v170, v85
	v_cvt_f32_i32_e32 v171, v82
	v_cvt_f32_i32_e32 v172, v80
	v_cvt_f32_i32_e32 v173, v81
	v_cvt_f32_i32_e32 v174, v79
	v_cvt_f32_i32_e32 v175, v77
	v_cvt_f32_i32_e32 v176, v76
	v_cvt_f32_i32_e32 v177, v73
	v_cvt_f32_i32_e32 v179, v72
	v_cvt_f32_i32_e32 v144, v78
	v_cvt_f32_i32_e32 v145, v83
	v_mov_b32_e32 v70, v212
	v_mov_b32_e32 v71, v213
	v_mov_b32_e32 v72, v214
	v_mov_b32_e32 v73, v215
	v_mov_b32_e32 v78, v216
	v_mov_b32_e32 v79, v217
	v_mov_b32_e32 v80, v218
	v_mov_b32_e32 v81, v219
	v_mov_b32_e32 v86, v220
	v_mov_b32_e32 v87, v221
	v_mov_b32_e32 v88, v222
	v_mov_b32_e32 v89, v223
	v_mov_b32_e32 v90, v224
	v_mov_b32_e32 v91, v225
	v_mov_b32_e32 v92, v226
	v_mov_b32_e32 v93, v227
	v_mov_b32_e32 v74, v228
	v_mov_b32_e32 v75, v229
	v_mov_b32_e32 v76, v230
	v_mov_b32_e32 v77, v231
	v_mov_b32_e32 v82, v232
	v_mov_b32_e32 v83, v233
	v_mov_b32_e32 v84, v234
	v_mov_b32_e32 v85, v235
	v_mov_b32_e32 v94, v236
	v_mov_b32_e32 v95, v237
	v_mov_b32_e32 v96, v238
	v_mov_b32_e32 v97, v239
	v_mov_b32_e32 v98, v240
	v_mov_b32_e32 v99, v241
	v_mov_b32_e32 v100, v242
	v_mov_b32_e32 v101, v243
	v_cvt_f32_i32_e32 v182, v66
	v_cvt_f32_i32_e32 v183, v69
	v_lshlrev_b64 v[154:155], 2, v[134:135]
	v_readlane_b32 s62, v255, 13
	v_lshl_add_u64 v[158:159], s[36:37], 0, v[154:155]
	v_readlane_b32 s63, v255, 14
	v_mul_f32_e32 v143, 0x3d800000, v142
	v_readlane_b32 s72, v254, 20
	v_lshl_add_u64 v[156:157], s[62:63], 0, v[154:155]
	v_readlane_b32 s73, v254, 21
	v_readlane_b32 s72, v255, 15
	v_readlane_b32 s73, v255, 16
	s_lshl_b64 s[62:63], s[86:87], 2
	v_readlane_b32 s74, v254, 22
	v_readlane_b32 s75, v254, 23
	s_add_u32 s62, s74, s62
	s_addc_u32 s63, s75, s63
	s_and_b64 vcc, exec, s[82:83]
	v_readlane_b32 s76, v254, 24
	v_readlane_b32 s77, v254, 25
	v_readlane_b32 s78, v254, 26
	v_readlane_b32 s79, v254, 27
	s_waitcnt vmcnt(0)
	v_readlane_b32 s98, v254, 58
	v_readlane_b32 s99, v255, 1
	s_cmp_lt_i32 s98, 0x4000
	s_cselect_b32 s100, s98, s88
	s_add_i32 s99, s98, s99
	s_cmp_lt_i32 s99, 0x4000
	s_cselect_b32 s99, s99, s100
	s_lshl_b32 s100, s100, 12
	s_lshl_b32 s99, s99, 9
	v_lshl_add_u32 v244, v130, 6, s100
	v_lshl_add_u32 v249, v130, 2, s99
	v_readlane_b32 s100, v255, 7
	v_readlane_b32 s101, v255, 9
	s_nop 4
	global_load_dwordx4 v[212:215], v244, s[100:101] offset:48
	global_load_dwordx4 v[216:219], v244, s[100:101] offset:32
	global_load_dwordx4 v[220:223], v244, s[100:101] offset:16
	global_load_dwordx4 v[224:227], v244, s[100:101]
	v_readlane_b32 s100, v254, 56
	v_readlane_b32 s101, v255, 5
	s_nop 4
	global_load_dwordx4 v[228:231], v244, s[100:101] offset:48
	global_load_dwordx4 v[232:235], v244, s[100:101] offset:32
	global_load_dwordx4 v[236:239], v244, s[100:101] offset:16
	global_load_dwordx4 v[240:243], v244, s[100:101]
	global_load_dword v245, v249, s[70:71] offset:256
	global_load_dword v246, v249, s[40:41] offset:256
	global_load_dword v247, v249, s[40:41]
	global_load_dword v248, v249, s[70:71]
	v_lshlrev_b32_e32 v66, 16, v98
	v_and_b32_e32 v69, 0xffff0000, v98
	v_lshlrev_b32_e32 v98, 16, v99
	v_and_b32_e32 v99, 0xffff0000, v99
	v_lshlrev_b32_e32 v164, 16, v100
	v_and_b32_e32 v165, 0xffff0000, v100
	v_lshlrev_b32_e32 v166, 16, v101
	v_and_b32_e32 v167, 0xffff0000, v101
	v_sub_f32_e32 v99, v99, v67
	v_sub_f32_e32 v98, v98, v67
	v_sub_f32_e32 v101, v69, v67
	v_sub_f32_e32 v100, v66, v67
	v_pk_mul_f32 v[184:185], v[68:69], v[100:101] op_sel_hi:[0,1]
	v_pk_mul_f32 v[186:187], v[68:69], v[98:99] op_sel_hi:[0,1]
	ds_read_b128 v[98:101], v154 offset:48
	ds_read_b128 v[102:105], v154 offset:32
	ds_read_b128 v[106:109], v154 offset:16
	ds_read_b128 v[122:125], v154 offset:0
	ds_read_b128 v[110:113], v154 offset:8240
	ds_read_b128 v[114:117], v154 offset:8224
	ds_read_b128 v[118:121], v154 offset:8208
	ds_read_b128 v[126:129], v154 offset:8192
	s_waitcnt lgkmcnt(0)
;     ...
;         for (int hh = 0; hh < 4; ++hh) { float pl[8]; unpack8(*(const v4u*)(PLE + (size_t)t * D + lane2 * 32 + hh * 8), pl);
;             float z8[8]; unpack8(*(const v4u*)(ZB + (size_t)t * D + lane2 * 32 + hh * 8), z8);
;             f32x4 xa = (f32x4){z8[0], z8[1], z8[2], z8[3]}, xb = (f32x4){z8[4], z8[5], z8[6], z8[7]};
;             xa = (xa - mean1) * rstd1 * *(const f32x4*)(gain1 + lane2 * 32 + hh * 8) + *(const f32x4*)(bias1 + lane2 * 32 + hh * 8);
;             xb = (xb - mean1) * rstd1 * *(const f32x4*)(gain1 + lane2 * 32 + hh * 8 + 4) + *(const f32x4*)(bias1 + lane2 * 32 + hh * 8 + 4);
;             acc[hh * 4 + 0] += (f32x2){ALPHA * xa[0] + pl[0], ALPHA * xa[1] + pl[1]}; acc[hh * 4 + 1] += (f32x2){ALPHA * xa[2] + pl[2], ALPHA * xa[3] + pl[3]};
;             acc[hh * 4 + 2] += (f32x2){ALPHA * xb[0] + pl[4], ALPHA * xb[1] + pl[5]}; acc[hh * 4 + 3] += (f32x2){ALPHA * xb[2] + pl[6], ALPHA * xb[3] + pl[7]};
; #pragma unroll
;             for (int i = 0; i < 4; ++i) s += acc[hh * 4 + i].x + acc[hh * 4 + i].y; }
	v_pk_fma_f32 v[124:125], v[124:125], v[186:187], v[128:129]
	v_sub_f32_e32 v129, v165, v67
	v_sub_f32_e32 v128, v164, v67
	v_pk_mul_f32 v[128:129], v[68:69], v[128:129] op_sel_hi:[0,1]
	v_pk_fma_f32 v[122:123], v[122:123], v[184:185], v[126:127]
	v_sub_f32_e32 v127, v167, v67
	v_sub_f32_e32 v126, v166, v67
	v_pk_fma_f32 v[106:107], v[106:107], v[128:129], v[118:119]
	v_lshlrev_b32_e32 v118, 16, v90
	v_and_b32_e32 v119, 0xffff0000, v90
	v_lshlrev_b32_e32 v90, 16, v91
	v_and_b32_e32 v91, 0xffff0000, v91
	v_pk_mul_f32 v[126:127], v[68:69], v[126:127] op_sel_hi:[0,1]
	v_pk_fma_f32 v[90:91], v[124:125], s[58:59], v[90:91] op_sel_hi:[1,0,1]
	v_pk_fma_f32 v[108:109], v[108:109], v[126:127], v[120:121]
	v_pk_fma_f32 v[118:119], v[122:123], s[58:59], v[118:119] op_sel_hi:[1,0,1]
	v_pk_fma_f32 v[120:121], v[142:143], v[180:181], v[90:91]
	v_lshlrev_b32_e32 v90, 16, v92
	v_and_b32_e32 v91, 0xffff0000, v92
	v_pk_fma_f32 v[118:119], v[142:143], v[182:183], v[118:119]
	v_pk_fma_f32 v[90:91], v[106:107], s[58:59], v[90:91] op_sel_hi:[1,0,1]
	v_add_f32_e32 v66, v118, v119
	v_pk_fma_f32 v[122:123], v[142:143], v[178:179], v[90:91]
	v_lshlrev_b32_e32 v90, 16, v93
	v_and_b32_e32 v91, 0xffff0000, v93
	v_pk_fma_f32 v[90:91], v[108:109], s[58:59], v[90:91] op_sel_hi:[1,0,1]
	v_add_f32_e32 v66, 0, v66
	v_add_f32_e32 v69, v120, v121
	v_pk_fma_f32 v[124:125], v[142:143], v[176:177], v[90:91]
	v_add_f32_e32 v66, v69, v66
	v_add_f32_e32 v69, v122, v123
	v_add_f32_e32 v66, v69, v66
	v_add_f32_e32 v69, v124, v125
	v_lshlrev_b32_e32 v90, 16, v95
	v_and_b32_e32 v91, 0xffff0000, v95
	v_lshlrev_b32_e32 v106, 16, v96
	v_and_b32_e32 v96, 0xffff0000, v96
	v_add_f32_e32 v66, v69, v66
	v_lshlrev_b32_e32 v69, 16, v94
	v_and_b32_e32 v92, 0xffff0000, v94
	v_lshlrev_b32_e32 v94, 16, v97
	v_and_b32_e32 v95, 0xffff0000, v97
	v_sub_f32_e32 v91, v91, v67
	v_sub_f32_e32 v90, v90, v67
	v_sub_f32_e32 v97, v96, v67
	v_sub_f32_e32 v96, v106, v67
	v_sub_f32_e32 v93, v92, v67
	v_sub_f32_e32 v92, v69, v67
	v_pk_mul_f32 v[90:91], v[68:69], v[90:91] op_sel_hi:[0,1]
	v_pk_mul_f32 v[96:97], v[68:69], v[96:97] op_sel_hi:[0,1]
	v_pk_mul_f32 v[92:93], v[68:69], v[92:93] op_sel_hi:[0,1]
	v_pk_fma_f32 v[90:91], v[104:105], v[90:91], v[116:117]
	v_pk_fma_f32 v[96:97], v[98:99], v[96:97], v[110:111]
	v_lshlrev_b32_e32 v98, 16, v86
	v_and_b32_e32 v99, 0xffff0000, v86
	v_lshlrev_b32_e32 v86, 16, v87
	v_and_b32_e32 v87, 0xffff0000, v87
	v_pk_fma_f32 v[92:93], v[102:103], v[92:93], v[114:115]
	v_pk_fma_f32 v[86:87], v[90:91], s[58:59], v[86:87] op_sel_hi:[1,0,1]
	v_sub_f32_e32 v95, v95, v67
	v_sub_f32_e32 v94, v94, v67
	v_pk_fma_f32 v[92:93], v[92:93], s[58:59], v[98:99] op_sel_hi:[1,0,1]
	v_pk_fma_f32 v[116:117], v[142:143], v[172:173], v[86:87]
	v_lshlrev_b32_e32 v86, 16, v88
	v_and_b32_e32 v87, 0xffff0000, v88
	v_pk_mul_f32 v[94:95], v[68:69], v[94:95] op_sel_hi:[0,1]
	v_pk_fma_f32 v[114:115], v[142:143], v[174:175], v[92:93]
	v_pk_fma_f32 v[86:87], v[96:97], s[58:59], v[86:87] op_sel_hi:[1,0,1]
	v_pk_fma_f32 v[94:95], v[100:101], v[94:95], v[112:113]
	v_pk_fma_f32 v[126:127], v[142:143], v[170:171], v[86:87]
	v_lshlrev_b32_e32 v86, 16, v89
	v_and_b32_e32 v87, 0xffff0000, v89
	v_add_f32_e32 v69, v114, v115
	v_pk_fma_f32 v[86:87], v[94:95], s[58:59], v[86:87] op_sel_hi:[1,0,1]
	v_add_f32_e32 v66, v66, v69
	v_add_f32_e32 v69, v116, v117
	v_pk_fma_f32 v[128:129], v[142:143], v[160:161], v[86:87]
	v_add_f32_e32 v66, v69, v66
	v_add_f32_e32 v69, v126, v127
	v_add_f32_e32 v66, v69, v66
	v_add_f32_e32 v69, v128, v129
	v_lshlrev_b32_e32 v86, 16, v82
	v_and_b32_e32 v87, 0xffff0000, v82
	v_lshlrev_b32_e32 v82, 16, v83
	v_and_b32_e32 v83, 0xffff0000, v83
	v_add_f32_e32 v66, v69, v66
	v_lshlrev_b32_e32 v69, 16, v84
	v_and_b32_e32 v172, 0xffff0000, v84
	v_lshlrev_b32_e32 v173, 16, v85
	v_and_b32_e32 v174, 0xffff0000, v85
	v_sub_f32_e32 v83, v83, v67
	v_sub_f32_e32 v82, v82, v67
	v_sub_f32_e32 v85, v87, v67
	v_sub_f32_e32 v84, v86, v67
	v_pk_mul_f32 v[160:161], v[68:69], v[84:85] op_sel_hi:[0,1]
	v_pk_mul_f32 v[170:171], v[68:69], v[82:83] op_sel_hi:[0,1]
	ds_read_b128 v[82:85], v154 offset:112
	ds_read_b128 v[86:89], v154 offset:96
	ds_read_b128 v[90:93], v154 offset:80
	ds_read_b128 v[106:109], v154 offset:64
	ds_read_b128 v[94:97], v154 offset:8304
	ds_read_b128 v[98:101], v154 offset:8288
	ds_read_b128 v[102:105], v154 offset:8272
	ds_read_b128 v[110:113], v154 offset:8256
	s_waitcnt lgkmcnt(0)
; __device__ __forceinline__ int fresh_lane() { unsigned z = 0u; asm volatile("" : "+v"(z)); return (int)__builtin_amdgcn_mbcnt_hi(~0u, __builtin_amdgcn_mbcnt_lo(~0u, z)); }
; __device__ __forceinline__ float shx(float v, int m, int lane) { return __builtin_bit_cast(float, shx_i(__builtin_bit_cast(int, v), m, lane)); }
; __device__ __forceinline__ float wave_sum(float v) {
;     const int l_ = fresh_lane();
; #pragma unroll
;     for (int o = 32; o >= 1; o >>= 1) v += shx(v, o, l_);
;     return v;
;     ...
;         for (int hh = 0; hh < 4; ++hh) { float pl[8]; unpack8(*(const v4u*)(PLE + (size_t)t * D + lane2 * 32 + hh * 8), pl);
;             float z8[8]; unpack8(*(const v4u*)(ZB + (size_t)t * D + lane2 * 32 + hh * 8), z8);
;             f32x4 xa = (f32x4){z8[0], z8[1], z8[2], z8[3]}, xb = (f32x4){z8[4], z8[5], z8[6], z8[7]};
;             xa = (xa - mean1) * rstd1 * *(const f32x4*)(gain1 + lane2 * 32 + hh * 8) + *(const f32x4*)(bias1 + lane2 * 32 + hh * 8);
;             xb = (xb - mean1) * rstd1 * *(const f32x4*)(gain1 + lane2 * 32 + hh * 8 + 4) + *(const f32x4*)(bias1 + lane2 * 32 + hh * 8 + 4);
;             acc[hh * 4 + 0] += (f32x2){ALPHA * xa[0] + pl[0], ALPHA * xa[1] + pl[1]}; acc[hh * 4 + 1] += (f32x2){ALPHA * xa[2] + pl[2], ALPHA * xa[3] + pl[3]};
;             acc[hh * 4 + 2] += (f32x2){ALPHA * xb[0] + pl[4], ALPHA * xb[1] + pl[5]}; acc[hh * 4 + 3] += (f32x2){ALPHA * xb[2] + pl[6], ALPHA * xb[3] + pl[7]};
; #pragma unroll
;             for (int i = 0; i < 4; ++i) s += acc[hh * 4 + i].x + acc[hh * 4 + i].y; }
;         const float mean = wave_sum(s) * (1.0f / D); float q = 0.f;
	v_pk_fma_f32 v[108:109], v[108:109], v[170:171], v[112:113]
	v_sub_f32_e32 v113, v172, v67
	v_sub_f32_e32 v112, v69, v67
	v_pk_mul_f32 v[112:113], v[68:69], v[112:113] op_sel_hi:[0,1]
	v_pk_fma_f32 v[106:107], v[106:107], v[160:161], v[110:111]
	v_sub_f32_e32 v111, v174, v67
	v_sub_f32_e32 v110, v173, v67
	v_pk_fma_f32 v[90:91], v[90:91], v[112:113], v[102:103]
	v_lshlrev_b32_e32 v102, 16, v78
	v_and_b32_e32 v103, 0xffff0000, v78
	v_lshlrev_b32_e32 v78, 16, v79
	v_and_b32_e32 v79, 0xffff0000, v79
	v_pk_mul_f32 v[110:111], v[68:69], v[110:111] op_sel_hi:[0,1]
	v_pk_fma_f32 v[78:79], v[108:109], s[58:59], v[78:79] op_sel_hi:[1,0,1]
	v_pk_fma_f32 v[92:93], v[92:93], v[110:111], v[104:105]
	v_pk_fma_f32 v[102:103], v[106:107], s[58:59], v[102:103] op_sel_hi:[1,0,1]
	v_pk_fma_f32 v[104:105], v[142:143], v[150:151], v[78:79]
	v_lshlrev_b32_e32 v78, 16, v80
	v_and_b32_e32 v79, 0xffff0000, v80
	v_pk_fma_f32 v[102:103], v[142:143], v[152:153], v[102:103]
	v_pk_fma_f32 v[78:79], v[90:91], s[58:59], v[78:79] op_sel_hi:[1,0,1]
	v_add_f32_e32 v69, v102, v103
	v_pk_fma_f32 v[90:91], v[142:143], v[148:149], v[78:79]
	v_lshlrev_b32_e32 v78, 16, v81
	v_and_b32_e32 v79, 0xffff0000, v81
	v_pk_fma_f32 v[78:79], v[92:93], s[58:59], v[78:79] op_sel_hi:[1,0,1]
	v_add_f32_e32 v66, v66, v69
	v_add_f32_e32 v69, v104, v105
	v_pk_fma_f32 v[92:93], v[142:143], v[146:147], v[78:79]
	v_add_f32_e32 v66, v69, v66
	v_add_f32_e32 v69, v90, v91
	v_add_f32_e32 v66, v69, v66
	v_add_f32_e32 v69, v92, v93
	v_add_f32_e32 v106, v69, v66
	v_lshlrev_b32_e32 v66, 16, v74
	v_and_b32_e32 v69, 0xffff0000, v74
	v_lshlrev_b32_e32 v74, 16, v75
	v_and_b32_e32 v75, 0xffff0000, v75
	v_lshlrev_b32_e32 v80, 16, v76
	v_and_b32_e32 v81, 0xffff0000, v76
	v_lshlrev_b32_e32 v78, 16, v77
	v_and_b32_e32 v79, 0xffff0000, v77
	v_sub_f32_e32 v75, v75, v67
	v_sub_f32_e32 v74, v74, v67
	v_sub_f32_e32 v77, v69, v67
	v_sub_f32_e32 v76, v66, v67
	v_pk_mul_f32 v[74:75], v[68:69], v[74:75] op_sel_hi:[0,1]
	v_sub_f32_e32 v79, v79, v67
	v_sub_f32_e32 v78, v78, v67
	v_sub_f32_e32 v81, v81, v67
	v_sub_f32_e32 v80, v80, v67
	v_pk_mul_f32 v[76:77], v[68:69], v[76:77] op_sel_hi:[0,1]
	v_pk_fma_f32 v[74:75], v[88:89], v[74:75], v[100:101]
	v_pk_mul_f32 v[66:67], v[68:69], v[80:81] op_sel_hi:[0,1]
	v_pk_mul_f32 v[68:69], v[68:69], v[78:79] op_sel_hi:[0,1]
	v_lshlrev_b32_e32 v78, 16, v70
	v_and_b32_e32 v79, 0xffff0000, v70
	v_lshlrev_b32_e32 v70, 16, v71
	v_and_b32_e32 v71, 0xffff0000, v71
	v_pk_fma_f32 v[76:77], v[86:87], v[76:77], v[98:99]
	v_pk_fma_f32 v[70:71], v[74:75], s[58:59], v[70:71] op_sel_hi:[1,0,1]
	v_pk_fma_f32 v[68:69], v[84:85], v[68:69], v[96:97]
	v_pk_fma_f32 v[66:67], v[82:83], v[66:67], v[94:95]
	v_pk_fma_f32 v[76:77], v[76:77], s[58:59], v[78:79] op_sel_hi:[1,0,1]
	v_pk_fma_f32 v[96:97], v[142:143], v[138:139], v[70:71]
	v_lshlrev_b32_e32 v70, 16, v72
	v_and_b32_e32 v71, 0xffff0000, v72
	v_pk_fma_f32 v[94:95], v[142:143], v[140:141], v[76:77]
	v_pk_fma_f32 v[66:67], v[66:67], s[58:59], v[70:71] op_sel_hi:[1,0,1]
	v_lshlrev_b32_e32 v70, 16, v73
	v_and_b32_e32 v71, 0xffff0000, v73
	v_pk_fma_f32 v[68:69], v[68:69], s[58:59], v[70:71] op_sel_hi:[1,0,1]
	v_mov_b32_e32 v70, v96
	v_mov_b32_e32 v71, v94
	v_mov_b32_e32 v72, v97
	v_mov_b32_e32 v73, v95
	v_pk_add_f32 v[70:71], v[70:71], v[72:73]
	v_pk_fma_f32 v[66:67], v[142:143], v[136:137], v[66:67]
	v_pk_fma_f32 v[68:69], v[142:143], v[144:145], v[68:69]
	v_add_f32_e32 v71, v106, v71
	v_add_f32_e32 v74, v70, v71
	v_mov_b32_e32 v70, v68
	v_mov_b32_e32 v71, v66
	v_mov_b32_e32 v72, v69
	v_mov_b32_e32 v73, v67
	v_pk_add_f32 v[70:71], v[70:71], v[72:73]
	v_lshl_add_u64 v[100:101], s[72:73], 0, v[154:155]
	v_add_f32_e32 v71, v71, v74
	v_add_f32_e32 v70, v70, v71
	v_mov_b32_e32 v71, v1
	v_lshl_add_u64 v[98:99], s[62:63], 0, v[154:155]
	v_mbcnt_lo_u32_b32 v71, -1, v71
	v_mbcnt_hi_u32_b32 v71, -1, v71
	v_lshlrev_b32_e32 v71, 2, v71
	v_xor_b32_e32 v72, 0x80, v71
	ds_bpermute_b32 v72, v72, v70
	s_waitcnt lgkmcnt(0)
	v_add_f32_e32 v70, v70, v72
	v_xor_b32_e32 v72, 64, v71
	ds_bpermute_b32 v72, v72, v70
	s_waitcnt lgkmcnt(0)
	v_add_f32_e32 v70, v70, v72
	v_xor_b32_e32 v72, 32, v71
	ds_bpermute_b32 v72, v72, v70
	s_waitcnt lgkmcnt(0)
	v_add_f32_e32 v70, v70, v72
	v_xor_b32_e32 v72, 16, v71
	ds_bpermute_b32 v72, v72, v70
	s_waitcnt lgkmcnt(0)
	v_add_f32_e32 v70, v70, v72
	v_xor_b32_e32 v72, 8, v71
	ds_bpermute_b32 v72, v72, v70
	v_xor_b32_e32 v71, 4, v71
	s_waitcnt lgkmcnt(0)
	v_add_f32_e32 v70, v70, v72
	ds_bpermute_b32 v71, v71, v70
	s_waitcnt lgkmcnt(0)
; __device__ __forceinline__ float ln_rstd(float q) { return __builtin_amdgcn_rsqf((q + LN_EPS * (float)D) * (1.0f / D)); }
; __device__ __forceinline__ v4u pack8(const float (&v)[8]) { v4u o; o.x = pk2(v[0], v[1]); o.y = pk2(v[2], v[3]); o.z = pk2(v[4], v[5]); o.w = pk2(v[6], v[7]); return o; }
;     ...
;         const float mean = wave_sum(s) * (1.0f / D); float q = 0.f;
; #pragma unroll
;         for (int i = 0; i < 16; ++i) { acc[i].x -= mean; acc[i].y -= mean; q += acc[i].x * acc[i].x + acc[i].y * acc[i].y; }
;         const float rstd = ln_rstd(wave_sum(q));
; #pragma unroll
;         for (int hh = 0; hh < 4; ++hh) {
;             const int c = lane2 * 32 + hh * 8;
;             float y[8];
; #pragma unroll
;             for (int q4 = 0; q4 < 2; ++q4) { const f32x4 ga = *(const f32x4*)(gain + c + q4 * 4), ba = *(const f32x4*)(bias + c + q4 * 4);
;                 const f32x2 z0 = acc[hh * 4 + q4 * 2], z1 = acc[hh * 4 + q4 * 2 + 1];
;                 f32x4 yo; yo[0] = z0.x * rstd * ga[0] + ba[0]; yo[1] = z0.y * rstd * ga[1] + ba[1]; yo[2] = z1.x * rstd * ga[2] + ba[2]; yo[3] = z1.y * rstd * ga[3] + ba[3];
;                 if (OF) *(f32x4*)(OF + (size_t)t * D + c + q4 * 4) = yo;
;                 y[q4 * 4] = yo[0]; y[q4 * 4 + 1] = yo[1]; y[q4 * 4 + 2] = yo[2]; y[q4 * 4 + 3] = yo[3]; }
;             if (!OF) *(v4u*)(XB + (size_t)t * D + c) = pack8(y);
	v_add_f32_e32 v70, v70, v71
	v_mul_f32_e32 v110, 0x3a000000, v70
	v_pk_add_f32 v[86:87], v[90:91], v[110:111] op_sel_hi:[1,0] neg_lo:[0,1] neg_hi:[0,1]
	v_pk_add_f32 v[88:89], v[92:93], v[110:111] op_sel_hi:[1,0] neg_lo:[0,1] neg_hi:[0,1]
	v_pk_add_f32 v[90:91], v[94:95], v[110:111] op_sel_hi:[1,0] neg_lo:[0,1] neg_hi:[0,1]
	v_pk_add_f32 v[92:93], v[96:97], v[110:111] op_sel_hi:[1,0] neg_lo:[0,1] neg_hi:[0,1]
	v_pk_add_f32 v[96:97], v[66:67], v[110:111] op_sel_hi:[1,0] neg_lo:[0,1] neg_hi:[0,1]
	v_pk_add_f32 v[94:95], v[68:69], v[110:111] op_sel_hi:[1,0] neg_lo:[0,1] neg_hi:[0,1]
	v_mov_b32_e32 v69, v97
	v_mov_b32_e32 v68, v95
	v_mov_b32_e32 v66, v94
	v_mov_b32_e32 v67, v96
	v_pk_mul_f32 v[68:69], v[68:69], v[68:69]
	v_pk_add_f32 v[82:83], v[102:103], v[110:111] op_sel_hi:[1,0] neg_lo:[0,1] neg_hi:[0,1]
	v_pk_fma_f32 v[144:145], v[66:67], v[66:67], v[68:69]
	v_mov_b32_e32 v66, v1
	v_lshl_add_u64 v[102:103], s[80:81], 0, v[154:155]
	v_mbcnt_lo_u32_b32 v66, -1, v66
	v_mbcnt_hi_u32_b32 v66, -1, v66
	v_lshlrev_b32_e32 v66, 2, v66
	v_xor_b32_e32 v148, 0x80, v66
	v_xor_b32_e32 v149, 64, v66
	v_xor_b32_e32 v150, 32, v66
	v_xor_b32_e32 v151, 16, v66
	v_xor_b32_e32 v152, 8, v66
	v_xor_b32_e32 v153, 4, v66
	ds_read_b128 v[66:69], v154 offset:16384
	ds_read_b128 v[106:109], v154 offset:24576
	v_pk_add_f32 v[70:71], v[122:123], v[110:111] op_sel_hi:[1,0] neg_lo:[0,1] neg_hi:[0,1]
	v_pk_add_f32 v[72:73], v[124:125], v[110:111] op_sel_hi:[1,0] neg_lo:[0,1] neg_hi:[0,1]
	v_pk_add_f32 v[74:75], v[114:115], v[110:111] op_sel_hi:[1,0] neg_lo:[0,1] neg_hi:[0,1]
	v_pk_add_f32 v[76:77], v[116:117], v[110:111] op_sel_hi:[1,0] neg_lo:[0,1] neg_hi:[0,1]
	v_pk_add_f32 v[78:79], v[126:127], v[110:111] op_sel_hi:[1,0] neg_lo:[0,1] neg_hi:[0,1]
	v_pk_add_f32 v[80:81], v[128:129], v[110:111] op_sel_hi:[1,0] neg_lo:[0,1] neg_hi:[0,1]
	v_pk_add_f32 v[84:85], v[104:105], v[110:111] op_sel_hi:[1,0] neg_lo:[0,1] neg_hi:[0,1]
	v_pk_add_f32 v[118:119], v[118:119], v[110:111] op_sel_hi:[1,0] neg_lo:[0,1] neg_hi:[0,1]
	v_pk_add_f32 v[110:111], v[120:121], v[110:111] op_sel_hi:[1,0] neg_lo:[0,1] neg_hi:[0,1]
	v_pk_mul_f32 v[146:147], v[118:119], v[118:119]
	v_pk_mul_f32 v[120:121], v[110:111], v[110:111]
	v_pk_mul_f32 v[112:113], v[70:71], v[70:71]
	v_add_f32_e32 v120, v120, v121
	v_add_f32_e32 v121, v146, v147
	v_pk_mul_f32 v[122:123], v[72:73], v[72:73]
	v_add_f32_e32 v120, v121, v120
	v_add_f32_e32 v112, v112, v113
	v_pk_mul_f32 v[114:115], v[74:75], v[74:75]
	v_add_f32_e32 v112, v112, v120
	v_add_f32_e32 v113, v122, v123
	v_pk_mul_f32 v[116:117], v[76:77], v[76:77]
	v_add_f32_e32 v112, v113, v112
	v_add_f32_e32 v113, v114, v115
	v_pk_mul_f32 v[124:125], v[78:79], v[78:79]
	v_add_f32_e32 v112, v113, v112
	v_add_f32_e32 v113, v116, v117
	v_pk_mul_f32 v[126:127], v[80:81], v[80:81]
	v_add_f32_e32 v112, v113, v112
	v_add_f32_e32 v113, v124, v125
	v_pk_mul_f32 v[128:129], v[82:83], v[82:83]
	v_add_f32_e32 v112, v113, v112
	v_add_f32_e32 v113, v126, v127
	v_pk_mul_f32 v[104:105], v[84:85], v[84:85]
	v_add_f32_e32 v112, v113, v112
	v_add_f32_e32 v113, v128, v129
	v_pk_mul_f32 v[136:137], v[86:87], v[86:87]
	v_add_f32_e32 v112, v113, v112
	v_add_f32_e32 v104, v104, v105
	v_pk_mul_f32 v[138:139], v[88:89], v[88:89]
	v_add_f32_e32 v104, v104, v112
	v_add_f32_e32 v105, v136, v137
	v_pk_mul_f32 v[140:141], v[90:91], v[90:91]
	v_add_f32_e32 v104, v105, v104
	v_add_f32_e32 v105, v138, v139
	v_pk_mul_f32 v[142:143], v[92:93], v[92:93]
	v_add_f32_e32 v104, v105, v104
	v_add_f32_e32 v105, v140, v141
	v_add_f32_e32 v104, v105, v104
	v_add_f32_e32 v105, v142, v143
	v_add_f32_e32 v104, v105, v104
	v_add_f32_e32 v104, v145, v104
	v_add_f32_e32 v104, v144, v104
	ds_bpermute_b32 v105, v148, v104
	s_waitcnt lgkmcnt(0)
	v_add_f32_e32 v104, v104, v105
	ds_bpermute_b32 v105, v149, v104
	s_waitcnt lgkmcnt(0)
	v_add_f32_e32 v104, v104, v105
	ds_bpermute_b32 v105, v150, v104
	s_waitcnt lgkmcnt(0)
	v_add_f32_e32 v104, v104, v105
	ds_bpermute_b32 v105, v151, v104
	s_waitcnt lgkmcnt(0)
	v_add_f32_e32 v104, v104, v105
	ds_bpermute_b32 v105, v152, v104
	s_waitcnt lgkmcnt(0)
	v_add_f32_e32 v104, v104, v105
	ds_bpermute_b32 v105, v153, v104
	s_waitcnt lgkmcnt(0)
	v_add_f32_e32 v104, v104, v105
	v_add_f32_e32 v104, 0x3ca7c5ac, v104
	v_mul_f32_e32 v104, 0x3a000000, v104
	v_rsq_f32_e32 v104, v104
	s_nop 0
	v_pk_mul_f32 v[112:113], v[118:119], v[104:105] op_sel_hi:[1,0]
	s_nop 0
	v_pk_fma_f32 v[66:67], v[66:67], v[112:113], v[106:107]
	v_pk_mul_f32 v[106:107], v[110:111], v[104:105] op_sel_hi:[1,0]
	s_nop 0
	v_pk_fma_f32 v[68:69], v[68:69], v[106:107], v[108:109]
	s_cbranch_vccz .LBB0_1428
	global_store_dwordx4 v[98:99], v[66:69], off
